# non-temporal (nt) cache policy on the wide global loads of phase 10 (RMSNorm rows) and phase 6 (post-scan); no other change
# speedup vs baseline: 1.1286x; 1.1286x over previous
_Z8mega_fwdILi0ELi16EEv4Args:
	s_mov_b64 s[84:85], s[0:1]
	s_load_dwordx4 s[60:63], s[0:1], 0xf0
	s_load_dword s93, s[0:1], 0x110
	s_add_u32 s0, s84, 0x110
	s_addc_u32 s1, s85, 0
	v_cmp_gt_u32_e32 vcc, 32, v0
	v_writelane_b32 v253, s0, 0
	s_nop 1
	v_writelane_b32 v253, s1, 1
	s_and_saveexec_b64 s[4:5], vcc
	v_lshl_add_u32 v1, v0, 2, 0
	v_add_u32_e32 v1, 0x24000, v1
	v_mov_b32_e32 v2, 0
	ds_write_b32 v1, v2
	s_or_b64 exec, exec, s[4:5]
	s_waitcnt lgkmcnt(0)
	s_barrier
	s_add_u32 s86, s62, 0x4000
	s_getreg_b32 s0, hwreg(HW_REG_XCC_ID, 0, 4)
	s_addc_u32 s87, s63, 0
	s_and_b32 s8, s0, 15
	v_cmp_eq_u32_e64 s[0:1], 0, v0
	s_mov_b64 s[4:5], exec
	s_nop 0
	v_writelane_b32 v253, s0, 2
	s_nop 1
	v_writelane_b32 v253, s1, 3
	s_and_b64 s[0:1], s[4:5], s[0:1]
	s_mov_b64 exec, s[0:1]
	s_cbranch_execz .LBB0_5
	s_mov_b64 s[6:7], exec
	v_mbcnt_lo_u32_b32 v1, s6, 0
	v_mbcnt_hi_u32_b32 v1, s7, v1
	v_cmp_eq_u32_e32 vcc, 0, v1
	s_and_b64 s[0:1], exec, vcc
	s_mov_b64 exec, s[0:1]
	s_cbranch_execz .LBB0_5
	s_lshl_b32 s0, s8, 8
	s_bcnt1_i32_b64 s1, s[6:7]
	v_mov_b32_e32 v1, s0
	v_mov_b32_e32 v2, s1
	global_atomic_add v1, v2, s[86:87] offset:1024

.LBB0_121:
	s_or_b64 exec, exec, s[18:19]
	s_lshl_b64 s[4:5], s[48:49], 11
	v_readlane_b32 s14, v253, 40
	v_writelane_b32 v252, s4, 39
	v_mov_b32_e32 v1, v0
	s_mov_b32 s16, s85
	s_mov_b64 s[26:27], s[62:63]
	s_waitcnt vmcnt(0)
	v_mov_b32_e32 v10, v0
	v_readlane_b32 s15, v253, 41
	v_writelane_b32 v252, s5, 40
	s_waitcnt lgkmcnt(0)
	s_barrier
	s_and_b64 vcc, exec, s[14:15]
	v_readfirstlane_b32 s4, v10
	s_cbranch_vccz .LBB0_149
	v_lshlrev_b32_e32 v1, 4, v10
	v_add_u32_e32 v2, 0x2000, v1
	v_ashrrev_i32_e32 v3, 31, v2
	v_lshrrev_b32_e32 v3, 22, v3
	v_add_u32_e32 v3, v2, v3
	v_ashrrev_i32_e32 v11, 10, v3
	v_mul_i32_i24_e32 v3, 0x400, v11
	v_sub_u32_e32 v2, v2, v3
	v_lshrrev_b32_e32 v3, 4, v2
	v_bitop3_b32 v2, v3, v2, 32 bitop3:0x6c
	v_ashrrev_i32_e32 v3, 31, v2
	v_lshrrev_b32_e32 v3, 26, v3
	v_add_u32_e32 v3, v2, v3
	v_lshlrev_b32_e32 v4, 3, v11
	v_ashrrev_i32_e32 v12, 6, v3
	v_and_b32_e32 v4, -16, v4
	v_add_u32_e32 v4, v12, v4
	v_and_b32_e32 v5, 3, v12
	s_mov_b32 s6, 0xfffe0
	v_lshrrev_b32_e32 v6, 2, v4
	v_lshlrev_b32_e32 v7, 1, v4
	v_and_b32_e32 v3, 0xc0, v3
	v_and_or_b32 v5, v4, s6, v5
	v_and_b32_e32 v6, 4, v6
	v_and_b32_e32 v7, 24, v7
	v_sub_u32_e32 v2, v2, v3
	v_or3_b32 v5, v5, v6, v7
	v_lshlrev_b32_e32 v6, 5, v11
	v_ashrrev_i16_sdwa v2, v215, sext(v2) dst_sel:DWORD dst_unused:UNUSED_PAD src0_sel:DWORD src1_sel:BYTE_0
	v_and_b32_e32 v6, 32, v6
	v_bfe_i32 v13, v2, 0, 16
	v_add_lshl_u32 v2, v6, v13, 1
	v_lshl_add_u32 v132, v5, 12, v2
	v_lshl_add_u32 v134, v4, 12, v2
	v_bfe_i32 v2, v10, 27, 1
	v_lshrrev_b32_e32 v2, 22, v2
	v_add_u32_e32 v2, v1, v2
	v_and_b32_e32 v2, 0xfffffc00, v2
	v_sub_u32_e32 v1, v1, v2
	v_lshrrev_b32_e32 v2, 4, v1
	v_ashrrev_i32_e32 v3, 31, v10
	v_bitop3_b32 v1, v2, v1, 32 bitop3:0x6c
	v_lshrrev_b32_e32 v3, 26, v3
	v_ashrrev_i32_e32 v2, 31, v1
	v_add_u32_e32 v3, v10, v3
	s_add_u32 s17, s26, 0x100000
	v_lshrrev_b32_e32 v2, 26, v2
	v_ashrrev_i32_e32 v15, 6, v3
	s_addc_u32 s44, s27, 0
	v_add_u32_e32 v2, v1, v2
	v_lshlrev_b32_e32 v3, 3, v15
	s_add_u32 s45, s26, 0x4800000
	v_ashrrev_i32_e32 v14, 6, v2
	v_and_b32_e32 v3, -16, v3
	s_addc_u32 s46, s27, 0
	s_ashr_i32 s14, s4, 6
	v_add_u32_e32 v3, v14, v3
	v_and_b32_e32 v4, 3, v14
	s_ashr_i32 s5, s4, 8
	s_lshl_b32 s47, s14, 10
	v_and_or_b32 v4, v3, s6, v4
	v_lshrrev_b32_e32 v5, 2, v3
	v_lshlrev_b32_e32 v6, 1, v3
	v_and_b32_e32 v2, 0xc0, v2
	v_readlane_b32 s6, v254, 35
	v_and_b32_e32 v5, 4, v5
	v_and_b32_e32 v6, 24, v6
	v_sub_u32_e32 v1, v1, v2
	v_readlane_b32 s7, v254, 36
	s_add_u32 s38, s17, s6
	v_or3_b32 v4, v4, v5, v6
	v_lshlrev_b32_e32 v5, 5, v15
	v_ashrrev_i16_sdwa v1, v215, sext(v1) dst_sel:DWORD dst_unused:UNUSED_PAD src0_sel:DWORD src1_sel:BYTE_0
	s_addc_u32 s39, s44, s7
	v_readlane_b32 s6, v254, 56
	v_and_b32_e32 v5, 32, v5
	v_bfe_i32 v16, v1, 0, 16
	v_readlane_b32 s7, v254, 57
	s_add_u32 s42, s45, s6
	v_add_lshl_u32 v1, v5, v16, 1
	s_addc_u32 s43, s46, s7
	s_add_i32 s48, s47, 0
	v_lshl_add_u32 v34, v4, 12, v1
	s_add_i32 m0, s48, 0x10000
	v_lshl_add_u32 v138, v3, 12, v1
	global_load_lds_dwordx4 v34, s[38:39]
	s_add_i32 m0, s48, 0x12000
	s_add_u32 s18, s38, 0x80000
	global_load_lds_dwordx4 v132, s[38:39]
	s_addc_u32 s19, s39, 0
	s_add_i32 m0, s48, 0x14000
	s_add_i32 s49, s48, 0x2000
	global_load_lds_dwordx4 v34, s[18:19]
	s_add_i32 m0, s48, 0x16000
	s_add_i32 s50, s48, 0x4000
	global_load_lds_dwordx4 v132, s[18:19]
	s_mov_b32 m0, s48
	v_add_u32_e32 v140, 0x80000, v138
	global_load_lds_dwordx4 v138, s[42:43]
	s_mov_b32 m0, s49
	s_add_i32 s51, s48, 0x6000
	global_load_lds_dwordx4 v134, s[42:43]
	s_mov_b32 m0, s50
	v_add_u32_e32 v136, 0x80000, v134
	global_load_lds_dwordx4 v140, s[42:43]
	s_mov_b32 m0, s51
	v_mov_b32_e32 v133, v35
	global_load_lds_dwordx4 v136, s[42:43]
	v_mov_b32_e32 v139, v35
	v_mov_b32_e32 v135, v35
	s_cmp_eq_u32 s5, 1
	v_lshl_add_u64 v[8:9], s[38:39], 0, v[34:35]
	v_lshl_add_u64 v[6:7], s[38:39], 0, v[132:133]
	v_lshl_add_u64 v[2:3], s[42:43], 0, v[138:139]
	s_cselect_b64 s[18:19], -1, 0
	s_cmp_lg_u32 s5, 1
	v_lshl_add_u64 v[4:5], s[42:43], 0, v[134:135]
	s_cbranch_scc1 .LBB0_124
	s_barrier

.LBB0_130:
	s_add_u32 s4, s38, 0x80
	s_addc_u32 s5, s39, 0
	s_add_i32 s31, 0, 0x10000
	s_cmp_eq_u32 s29, 28
	s_cselect_b32 s5, s35, s5
	s_cselect_b32 s4, s34, s4
	v_add_u32_e32 v146, s31, v148
	s_cselect_b32 s43, s37, s15
	s_cselect_b32 s42, s36, s14
	s_add_i32 s68, 0, 0x14000
	ds_read_b128 v[152:155], v146
	ds_read_b128 v[156:159], v146 offset:1024
	ds_read_b128 v[160:163], v146 offset:2048
	ds_read_b128 v[164:167], v146 offset:3072
	v_add_u32_e32 v146, s68, v148
	ds_read_b128 v[168:171], v146
	ds_read_b128 v[172:175], v146 offset:1024
	ds_read_b128 v[176:179], v146 offset:2048
	ds_read_b128 v[180:183], v146 offset:3072
	v_lshl_add_u64 v[146:147], s[38:39], 0, v[144:145]
	s_add_i32 m0, s48, 0xc000
	ds_read_b128 v[184:187], v150
	ds_read_b128 v[188:191], v150 offset:1024
	ds_read_b128 v[192:195], v150 offset:2048
	ds_read_b128 v[196:199], v150 offset:3072
	ds_read_b128 v[224:227], v150 offset:4096
	ds_read_b128 v[228:231], v150 offset:5120
	ds_read_b128 v[238:241], v150 offset:6144
	ds_read_b128 v[242:245], v150 offset:7168
	global_load_lds_dwordx4 v[146:147], off
	v_lshl_add_u64 v[146:147], s[38:39], 0, v[142:143]
	s_add_i32 m0, s48, 0xe000
	s_nop 0
	global_load_lds_dwordx4 v[146:147], off
	s_waitcnt vmcnt(8)
	s_waitcnt lgkmcnt(0)
	s_barrier
	s_setprio 1
	s_waitcnt lgkmcnt(0)
	v_mfma_f32_16x16x32_bf16 v[128:131], v[152:155], v[184:187], v[128:131]
	v_mfma_f32_16x16x32_bf16 v[124:127], v[160:163], v[184:187], v[124:127]
	v_mfma_f32_16x16x32_bf16 v[120:123], v[152:155], v[192:195], v[120:123]
	v_mfma_f32_16x16x32_bf16 v[112:115], v[160:163], v[192:195], v[112:115]
	v_mfma_f32_16x16x32_bf16 v[104:107], v[152:155], v[224:227], v[104:107]
	v_mfma_f32_16x16x32_bf16 v[96:99], v[160:163], v[224:227], v[96:99]
	v_mfma_f32_16x16x32_bf16 v[88:91], v[152:155], v[238:241], v[88:91]
	v_mfma_f32_16x16x32_bf16 v[80:83], v[160:163], v[238:241], v[80:83]
	v_mfma_f32_16x16x32_bf16 v[128:131], v[156:159], v[188:191], v[128:131]
	v_mfma_f32_16x16x32_bf16 v[124:127], v[164:167], v[188:191], v[124:127]
	v_mfma_f32_16x16x32_bf16 v[120:123], v[156:159], v[196:199], v[120:123]
	v_mfma_f32_16x16x32_bf16 v[112:115], v[164:167], v[196:199], v[112:115]
	v_mfma_f32_16x16x32_bf16 v[104:107], v[156:159], v[228:231], v[104:107]
	v_mfma_f32_16x16x32_bf16 v[96:99], v[164:167], v[228:231], v[96:99]
	v_mfma_f32_16x16x32_bf16 v[88:91], v[156:159], v[242:245], v[88:91]
	v_mfma_f32_16x16x32_bf16 v[80:83], v[164:167], v[242:245], v[80:83]
	s_setprio 0
	s_setprio 1
	v_mfma_f32_16x16x32_bf16 v[116:119], v[168:171], v[184:187], v[116:119]
	v_mfma_f32_16x16x32_bf16 v[108:111], v[176:179], v[184:187], v[108:111]
	v_mfma_f32_16x16x32_bf16 v[100:103], v[168:171], v[192:195], v[100:103]
	v_mfma_f32_16x16x32_bf16 v[92:95], v[176:179], v[192:195], v[92:95]
	v_mfma_f32_16x16x32_bf16 v[84:87], v[168:171], v[224:227], v[84:87]
	v_mfma_f32_16x16x32_bf16 v[76:79], v[176:179], v[224:227], v[76:79]
	v_mfma_f32_16x16x32_bf16 v[72:75], v[168:171], v[238:241], v[72:75]
	v_mfma_f32_16x16x32_bf16 v[68:71], v[176:179], v[238:241], v[68:71]
	v_mfma_f32_16x16x32_bf16 v[116:119], v[172:175], v[188:191], v[116:119]
	v_mfma_f32_16x16x32_bf16 v[108:111], v[180:183], v[188:191], v[108:111]
	v_mfma_f32_16x16x32_bf16 v[100:103], v[172:175], v[196:199], v[100:103]
	v_mfma_f32_16x16x32_bf16 v[92:95], v[180:183], v[196:199], v[92:95]
	v_mfma_f32_16x16x32_bf16 v[84:87], v[172:175], v[228:231], v[84:87]
	v_mfma_f32_16x16x32_bf16 v[76:79], v[180:183], v[228:231], v[76:79]
	v_mfma_f32_16x16x32_bf16 v[72:75], v[172:175], v[242:245], v[72:75]
	v_mfma_f32_16x16x32_bf16 v[68:71], v[180:183], v[242:245], v[68:71]
	s_setprio 0
	s_barrier
	s_add_i32 s31, s31, s47
	v_lshl_add_u64 v[146:147], s[42:43], 0, v[34:35]
	s_mov_b32 m0, s31
	ds_read_b128 v[184:187], v150 offset:16384
	ds_read_b128 v[188:191], v150 offset:17408
	ds_read_b128 v[192:195], v150 offset:18432
	ds_read_b128 v[196:199], v150 offset:19456
	ds_read_b128 v[224:227], v150 offset:20480
	ds_read_b128 v[228:231], v150 offset:21504
	ds_read_b128 v[238:241], v150 offset:22528
	ds_read_b128 v[242:245], v150 offset:23552
	global_load_lds_dwordx4 v[146:147], off
	s_add_i32 m0, s31, 0x2000
	s_add_u32 s64, s42, 0x80000
	v_lshl_add_u64 v[212:213], s[42:43], 0, v[132:133]
	s_addc_u32 s65, s43, 0
	s_add_i32 s31, s68, s47
	global_load_lds_dwordx4 v[212:213], off
	v_lshl_add_u64 v[232:233], s[64:65], 0, v[34:35]
	s_mov_b32 m0, s31
	v_lshl_add_u64 v[246:247], s[4:5], 0, v[134:135]
	global_load_lds_dwordx4 v[232:233], off
	v_lshl_add_u64 v[232:233], s[64:65], 0, v[132:133]
	s_add_i32 m0, s31, 0x2000
	s_nop 0
	global_load_lds_dwordx4 v[232:233], off
	v_lshl_add_u64 v[232:233], s[4:5], 0, v[138:139]
	s_mov_b32 m0, s48
	s_nop 0
	global_load_lds_dwordx4 v[232:233], off
	s_mov_b32 m0, s49
	s_nop 0
	global_load_lds_dwordx4 v[246:247], off
	s_waitcnt vmcnt(8)
	s_waitcnt lgkmcnt(0)
	s_barrier
	s_setprio 1
	s_waitcnt lgkmcnt(0)
	v_mfma_f32_16x16x32_bf16 v[64:67], v[152:155], v[184:187], v[64:67]
	v_mfma_f32_16x16x32_bf16 v[60:63], v[160:163], v[184:187], v[60:63]
	v_mfma_f32_16x16x32_bf16 v[52:55], v[152:155], v[192:195], v[52:55]
	v_mfma_f32_16x16x32_bf16 v[44:47], v[160:163], v[192:195], v[44:47]
	v_mfma_f32_16x16x32_bf16 v[36:39], v[152:155], v[224:227], v[36:39]
	v_mfma_f32_16x16x32_bf16 v[26:29], v[160:163], v[224:227], v[26:29]
	v_mfma_f32_16x16x32_bf16 v[18:21], v[152:155], v[238:241], v[18:21]
	v_mfma_f32_16x16x32_bf16 v[10:13], v[160:163], v[238:241], v[10:13]
	v_mfma_f32_16x16x32_bf16 v[64:67], v[156:159], v[188:191], v[64:67]
	v_mfma_f32_16x16x32_bf16 v[60:63], v[164:167], v[188:191], v[60:63]
	v_mfma_f32_16x16x32_bf16 v[52:55], v[156:159], v[196:199], v[52:55]
	v_mfma_f32_16x16x32_bf16 v[44:47], v[164:167], v[196:199], v[44:47]
	v_mfma_f32_16x16x32_bf16 v[36:39], v[156:159], v[228:231], v[36:39]
	v_mfma_f32_16x16x32_bf16 v[26:29], v[164:167], v[228:231], v[26:29]
	v_mfma_f32_16x16x32_bf16 v[18:21], v[156:159], v[242:245], v[18:21]
	v_mfma_f32_16x16x32_bf16 v[10:13], v[164:167], v[242:245], v[10:13]
	s_setprio 0
	s_setprio 1
	v_mfma_f32_16x16x32_bf16 v[56:59], v[168:171], v[184:187], v[56:59]
	v_mfma_f32_16x16x32_bf16 v[48:51], v[176:179], v[184:187], v[48:51]
	v_mfma_f32_16x16x32_bf16 v[40:43], v[168:171], v[192:195], v[40:43]
	v_mfma_f32_16x16x32_bf16 v[30:33], v[176:179], v[192:195], v[30:33]
	v_mfma_f32_16x16x32_bf16 v[22:25], v[168:171], v[224:227], v[22:25]
	v_mfma_f32_16x16x32_bf16 v[14:17], v[176:179], v[224:227], v[14:17]
	v_mfma_f32_16x16x32_bf16 v[6:9], v[168:171], v[238:241], v[6:9]
	v_mfma_f32_16x16x32_bf16 v[2:5], v[176:179], v[238:241], v[2:5]
	v_mfma_f32_16x16x32_bf16 v[56:59], v[172:175], v[188:191], v[56:59]
	v_mfma_f32_16x16x32_bf16 v[48:51], v[180:183], v[188:191], v[48:51]
	v_mfma_f32_16x16x32_bf16 v[40:43], v[172:175], v[196:199], v[40:43]
	v_mfma_f32_16x16x32_bf16 v[30:33], v[180:183], v[196:199], v[30:33]
	v_mfma_f32_16x16x32_bf16 v[22:25], v[172:175], v[228:231], v[22:25]
	v_mfma_f32_16x16x32_bf16 v[14:17], v[180:183], v[228:231], v[14:17]
	v_mfma_f32_16x16x32_bf16 v[6:9], v[172:175], v[242:245], v[6:9]
	v_mfma_f32_16x16x32_bf16 v[2:5], v[180:183], v[242:245], v[2:5]
	s_setprio 0
	s_barrier
	s_add_i32 s31, 0, 0x18000
	v_add_u32_e32 v151, s31, v148
	s_add_i32 s64, 0, 0x1c000
	ds_read_b128 v[152:155], v151
	ds_read_b128 v[156:159], v151 offset:1024
	ds_read_b128 v[160:163], v151 offset:2048
	ds_read_b128 v[164:167], v151 offset:3072
	v_add_u32_e32 v151, s64, v148
	ds_read_b128 v[168:171], v151
	ds_read_b128 v[172:175], v151 offset:1024
	ds_read_b128 v[176:179], v151 offset:2048
	ds_read_b128 v[180:183], v151 offset:3072
	s_mov_b32 m0, s50
	v_lshl_add_u64 v[248:249], s[4:5], 0, v[140:141]
	ds_read_b128 v[184:187], v150 offset:32768
	ds_read_b128 v[188:191], v150 offset:33792
	ds_read_b128 v[192:195], v150 offset:34816
	ds_read_b128 v[196:199], v150 offset:35840
	ds_read_b128 v[224:227], v150 offset:36864
	ds_read_b128 v[228:231], v150 offset:37888
	ds_read_b128 v[238:241], v150 offset:38912
	ds_read_b128 v[242:245], v150 offset:39936
	global_load_lds_dwordx4 v[248:249], off
	v_lshl_add_u64 v[248:249], s[4:5], 0, v[136:137]
	s_mov_b32 m0, s51
	s_nop 0
	global_load_lds_dwordx4 v[248:249], off
	s_waitcnt vmcnt(8)
	s_waitcnt lgkmcnt(0)
	s_barrier
	s_setprio 1
	s_waitcnt lgkmcnt(0)
	v_mfma_f32_16x16x32_bf16 v[128:131], v[152:155], v[184:187], v[128:131]
	v_mfma_f32_16x16x32_bf16 v[124:127], v[160:163], v[184:187], v[124:127]
	v_mfma_f32_16x16x32_bf16 v[120:123], v[152:155], v[192:195], v[120:123]
	v_mfma_f32_16x16x32_bf16 v[112:115], v[160:163], v[192:195], v[112:115]
	v_mfma_f32_16x16x32_bf16 v[104:107], v[152:155], v[224:227], v[104:107]
	v_mfma_f32_16x16x32_bf16 v[96:99], v[160:163], v[224:227], v[96:99]
	v_mfma_f32_16x16x32_bf16 v[88:91], v[152:155], v[238:241], v[88:91]
	v_mfma_f32_16x16x32_bf16 v[80:83], v[160:163], v[238:241], v[80:83]
	v_mfma_f32_16x16x32_bf16 v[128:131], v[156:159], v[188:191], v[128:131]
	v_mfma_f32_16x16x32_bf16 v[124:127], v[164:167], v[188:191], v[124:127]
	v_mfma_f32_16x16x32_bf16 v[120:123], v[156:159], v[196:199], v[120:123]
	v_mfma_f32_16x16x32_bf16 v[112:115], v[164:167], v[196:199], v[112:115]
	v_mfma_f32_16x16x32_bf16 v[104:107], v[156:159], v[228:231], v[104:107]
	v_mfma_f32_16x16x32_bf16 v[96:99], v[164:167], v[228:231], v[96:99]
	v_mfma_f32_16x16x32_bf16 v[88:91], v[156:159], v[242:245], v[88:91]
	v_mfma_f32_16x16x32_bf16 v[80:83], v[164:167], v[242:245], v[80:83]
	s_setprio 0
	s_setprio 1
	v_mfma_f32_16x16x32_bf16 v[116:119], v[168:171], v[184:187], v[116:119]
	v_mfma_f32_16x16x32_bf16 v[108:111], v[176:179], v[184:187], v[108:111]
	v_mfma_f32_16x16x32_bf16 v[100:103], v[168:171], v[192:195], v[100:103]
	v_mfma_f32_16x16x32_bf16 v[92:95], v[176:179], v[192:195], v[92:95]
	v_mfma_f32_16x16x32_bf16 v[84:87], v[168:171], v[224:227], v[84:87]
	v_mfma_f32_16x16x32_bf16 v[76:79], v[176:179], v[224:227], v[76:79]
	v_mfma_f32_16x16x32_bf16 v[72:75], v[168:171], v[238:241], v[72:75]
	v_mfma_f32_16x16x32_bf16 v[68:71], v[176:179], v[238:241], v[68:71]
	v_mfma_f32_16x16x32_bf16 v[116:119], v[172:175], v[188:191], v[116:119]
	v_mfma_f32_16x16x32_bf16 v[108:111], v[180:183], v[188:191], v[108:111]
	v_mfma_f32_16x16x32_bf16 v[100:103], v[172:175], v[196:199], v[100:103]
	v_mfma_f32_16x16x32_bf16 v[92:95], v[180:183], v[196:199], v[92:95]
	v_mfma_f32_16x16x32_bf16 v[84:87], v[172:175], v[228:231], v[84:87]
	v_mfma_f32_16x16x32_bf16 v[76:79], v[180:183], v[228:231], v[76:79]
	v_mfma_f32_16x16x32_bf16 v[72:75], v[172:175], v[242:245], v[72:75]
	v_mfma_f32_16x16x32_bf16 v[68:71], v[180:183], v[242:245], v[68:71]
	s_setprio 0
	s_barrier
	s_add_i32 s4, s31, s47
	v_lshl_add_u64 v[146:147], v[146:147], 0, s[78:79]
	s_mov_b32 m0, s4
	ds_read_b128 v[184:187], v150 offset:49152
	ds_read_b128 v[188:191], v150 offset:50176
	ds_read_b128 v[192:195], v150 offset:51200
	ds_read_b128 v[196:199], v150 offset:52224
	ds_read_b128 v[224:227], v150 offset:53248
	ds_read_b128 v[228:231], v150 offset:54272
	ds_read_b128 v[238:241], v150 offset:55296
	ds_read_b128 v[242:245], v150 offset:56320
	global_load_lds_dwordx4 v[146:147], off
	s_add_i32 m0, s4, 0x2000
	s_add_u32 s4, s42, 0x80080
	v_lshl_add_u64 v[146:147], v[212:213], 0, s[78:79]
	s_addc_u32 s5, s43, 0
	s_add_i32 s31, s64, s47
	global_load_lds_dwordx4 v[146:147], off
	v_lshl_add_u64 v[146:147], s[4:5], 0, v[34:35]
	s_mov_b32 m0, s31
	s_nop 0
	global_load_lds_dwordx4 v[146:147], off
	v_lshl_add_u64 v[146:147], s[4:5], 0, v[132:133]
	s_add_i32 m0, s31, 0x2000
	s_nop 0
	global_load_lds_dwordx4 v[146:147], off
	v_lshl_add_u64 v[146:147], v[232:233], 0, s[78:79]
	s_mov_b32 m0, s52
	s_nop 0
	global_load_lds_dwordx4 v[146:147], off
	v_lshl_add_u64 v[146:147], v[246:247], 0, s[78:79]
	s_mov_b32 m0, s53
	s_nop 0
	global_load_lds_dwordx4 v[146:147], off
	s_waitcnt vmcnt(8)
	s_waitcnt lgkmcnt(0)
	s_barrier
	s_setprio 1
	s_waitcnt lgkmcnt(0)
	v_mfma_f32_16x16x32_bf16 v[64:67], v[152:155], v[184:187], v[64:67]
	v_mfma_f32_16x16x32_bf16 v[60:63], v[160:163], v[184:187], v[60:63]
	v_mfma_f32_16x16x32_bf16 v[52:55], v[152:155], v[192:195], v[52:55]
	v_mfma_f32_16x16x32_bf16 v[44:47], v[160:163], v[192:195], v[44:47]
	v_mfma_f32_16x16x32_bf16 v[36:39], v[152:155], v[224:227], v[36:39]
	v_mfma_f32_16x16x32_bf16 v[26:29], v[160:163], v[224:227], v[26:29]
	v_mfma_f32_16x16x32_bf16 v[18:21], v[152:155], v[238:241], v[18:21]
	v_mfma_f32_16x16x32_bf16 v[10:13], v[160:163], v[238:241], v[10:13]
	v_mfma_f32_16x16x32_bf16 v[64:67], v[156:159], v[188:191], v[64:67]
	v_mfma_f32_16x16x32_bf16 v[60:63], v[164:167], v[188:191], v[60:63]
	v_mfma_f32_16x16x32_bf16 v[52:55], v[156:159], v[196:199], v[52:55]
	v_mfma_f32_16x16x32_bf16 v[44:47], v[164:167], v[196:199], v[44:47]
	v_mfma_f32_16x16x32_bf16 v[36:39], v[156:159], v[228:231], v[36:39]
	v_mfma_f32_16x16x32_bf16 v[26:29], v[164:167], v[228:231], v[26:29]
	v_mfma_f32_16x16x32_bf16 v[18:21], v[156:159], v[242:245], v[18:21]
	v_mfma_f32_16x16x32_bf16 v[10:13], v[164:167], v[242:245], v[10:13]
	s_setprio 0
	s_setprio 1
	v_mfma_f32_16x16x32_bf16 v[56:59], v[168:171], v[184:187], v[56:59]
	v_mfma_f32_16x16x32_bf16 v[48:51], v[176:179], v[184:187], v[48:51]
	v_mfma_f32_16x16x32_bf16 v[40:43], v[168:171], v[192:195], v[40:43]
	v_mfma_f32_16x16x32_bf16 v[30:33], v[176:179], v[192:195], v[30:33]
	v_mfma_f32_16x16x32_bf16 v[22:25], v[168:171], v[224:227], v[22:25]
	v_mfma_f32_16x16x32_bf16 v[14:17], v[176:179], v[224:227], v[14:17]
	v_mfma_f32_16x16x32_bf16 v[6:9], v[168:171], v[238:241], v[6:9]
	v_mfma_f32_16x16x32_bf16 v[2:5], v[176:179], v[238:241], v[2:5]
	v_mfma_f32_16x16x32_bf16 v[56:59], v[172:175], v[188:191], v[56:59]
	v_mfma_f32_16x16x32_bf16 v[48:51], v[180:183], v[188:191], v[48:51]
	v_mfma_f32_16x16x32_bf16 v[40:43], v[172:175], v[196:199], v[40:43]
	v_mfma_f32_16x16x32_bf16 v[30:33], v[180:183], v[196:199], v[30:33]
	v_mfma_f32_16x16x32_bf16 v[22:25], v[172:175], v[228:231], v[22:25]
	v_mfma_f32_16x16x32_bf16 v[14:17], v[180:183], v[228:231], v[14:17]
	v_mfma_f32_16x16x32_bf16 v[6:9], v[172:175], v[242:245], v[6:9]
	v_mfma_f32_16x16x32_bf16 v[2:5], v[180:183], v[242:245], v[2:5]
	s_setprio 0
	s_barrier
	s_add_i32 s29, s29, 2
	s_add_u32 s14, s14, 0x100
	s_addc_u32 s15, s15, 0
	s_add_u32 s38, s38, 0x100
	s_addc_u32 s39, s39, 0
	s_cmp_gt_u32 s29, 29
	s_cbranch_scc0 .LBB0_130
	s_and_b64 vcc, exec, s[22:23]
	s_cbranch_vccz .LBB0_133
	s_barrier

.LBB0_193:
	s_or_b64 exec, exec, s[18:19]
	v_mov_b32_e32 v2, v0
	s_waitcnt lgkmcnt(0)
	s_barrier
	s_mov_b32 s27, s85
	v_readfirstlane_b32 s4, v2
	s_ashr_i32 s26, s4, 6
	v_readlane_b32 s4, v253, 62
	s_add_i32 s16, s26, s4
	s_mov_b64 s[4:5], s[62:63]
	s_mov_b32 s24, 4
	s_mov_b32 s22, 10
	s_mov_b32 s20, 17
	s_mov_b32 s18, 18
	s_mov_b32 s14, 1
	s_cmpk_lt_i32 s16, 0x800
	s_cbranch_scc0 .LBB0_269
	s_lshl_b32 s17, s27, 3
	s_add_u32 s30, s4, 0xc800000
	s_addc_u32 s31, s5, 0
	s_add_u32 s34, s4, 0x3c800000
	s_addc_u32 s35, s5, 0
	s_ashr_i32 s25, s24, 31
	s_lshl_b64 s[24:25], s[24:25], 3
	s_add_u32 s24, s70, s24
	s_addc_u32 s25, s71, s25
	s_ashr_i32 s23, s22, 31
	s_lshl_b64 s[22:23], s[22:23], 3
	s_add_u32 s22, s70, s22
	s_addc_u32 s23, s71, s23
	s_ashr_i32 s21, s20, 31
	s_lshl_b64 s[20:21], s[20:21], 3
	s_add_u32 s20, s70, s20
	s_addc_u32 s21, s71, s21
	s_ashr_i32 s19, s18, 31
	s_lshl_b64 s[18:19], s[18:19], 3
	s_add_u32 s18, s70, s18
	s_addc_u32 s19, s71, s19
	s_load_dwordx2 s[24:25], s[24:25], 0x0
	s_nop 0
	s_load_dwordx2 s[22:23], s[22:23], 0x0
	s_nop 0
	s_load_dwordx2 s[20:21], s[20:21], 0x0
	s_nop 0
	s_load_dwordx2 s[28:29], s[18:19], 0x0
	s_ashr_i32 s15, s14, 31
	s_lshl_b64 s[14:15], s[14:15], 3
	s_add_u32 s14, s70, s14
	v_readlane_b32 s6, v252, 35
	s_addc_u32 s15, s71, s15
	v_readlane_b32 s7, v252, 36
	s_load_dwordx2 s[18:19], s[14:15], 0x0
	s_lshl_b64 s[14:15], s[6:7], 8
	s_waitcnt lgkmcnt(0)
	s_add_u32 s28, s28, s14
	s_addc_u32 s29, s29, s15
	s_add_u32 s36, s20, s14
	s_addc_u32 s37, s21, s15
	v_readlane_b32 s14, v252, 37
	v_readlane_b32 s15, v252, 38
	s_lshl_b64 s[14:15], s[14:15], 2
	s_add_u32 s22, s22, s14
	v_and_b32_e32 v13, 31, v2
	s_addc_u32 s23, s23, s15
	s_mul_i32 s14, s6, 0x3700
	v_cvt_f32_ubyte0_e32 v14, v13
	s_add_u32 s14, s24, s14
	v_mul_f32_e32 v15, 0xbed49a78, v14
	s_mov_b32 s24, 0xc2fc0000
	v_cmp_gt_f32_e32 vcc, s24, v15
	v_mov_b32_e32 v15, 0x42800000
	s_mul_hi_i32 s15, s6, 0x3700
	v_cndmask_b32_e32 v15, 0, v15, vcc
	v_fmac_f32_e32 v15, 0xbed49a78, v14
	s_addc_u32 s15, s25, s15
	v_and_b32_e32 v3, 63, v2
	v_exp_f32_e32 v14, v15
	v_or_b32_e32 v5, 64, v3
	s_add_u32 s20, s4, 0x1a800000
	s_addc_u32 s21, s5, 0
	v_lshlrev_b32_e32 v34, 4, v3
	v_lshrrev_b32_e32 v9, 5, v5
	v_lshl_add_u64 v[106:107], s[20:21], 0, v[34:35]
	v_lshlrev_b32_e64 v105, v9, 2
	v_lshlrev_b32_e32 v34, 4, v5
	v_cmp_ne_u32_e64 s[44:45], 3, v9
	v_cndmask_b32_e32 v9, 0, v219, vcc
	v_lshl_add_u64 v[108:109], s[20:21], 0, v[34:35]
	v_ldexp_f32 v148, v14, v9
	v_lshlrev_b32_e32 v34, 2, v13
	v_lshlrev_b32_e32 v9, 4, v2
	v_lshlrev_b32_e32 v4, 3, v3
	v_lshlrev_b32_e32 v8, 5, v3
	v_or_b32_e32 v7, 0x180, v3
	v_cmp_gt_u32_e64 s[40:41], 56, v3
	v_cmp_gt_u32_e64 s[42:43], 32, v3
	v_lshl_add_u64 v[110:111], s[36:37], 0, v[34:35]
	v_lshl_add_u64 v[112:113], s[28:29], 0, v[34:35]
	v_and_b32_e32 v34, 0x70, v9
	v_cmp_gt_u32_e64 s[46:47], 40, v3
	v_cmp_gt_u32_e32 vcc, 20, v3
	v_mov_b32_e32 v3, 0xc0
	v_mov_b32_e32 v9, 0x60
	v_cndmask_b32_e32 v3, v3, v9, vcc
	v_mov_b32_e32 v9, v35
	v_or_b32_e32 v10, 0x800, v4
	v_lshl_add_u64 v[114:115], s[14:15], 0, v[8:9]
	v_lshl_add_u64 v[116:117], s[22:23], 0, v[8:9]
	v_or_b32_e32 v18, 0x1000, v8
	v_or_b32_e32 v8, 0x1800, v8
	v_or_b32_e32 v12, 0xa00, v4
	v_lshl_add_u64 v[122:123], s[14:15], 0, v[8:9]
	v_lshlrev_b32_e32 v8, 2, v10
	v_lshl_add_u64 v[126:127], s[14:15], 0, v[8:9]
	v_lshlrev_b32_e32 v8, 2, v12
	v_bfe_u32 v11, v2, 5, 1
	v_lshlrev_b32_e32 v16, 5, v5
	v_mov_b32_e32 v17, v35
	v_mov_b32_e32 v19, v35
	v_lshl_add_u64 v[128:129], s[14:15], 0, v[8:9]
	v_lshlrev_b32_e32 v8, 5, v7
	v_lshl_add_u64 v[118:119], s[14:15], 0, v[16:17]
	v_lshl_add_u64 v[120:121], s[14:15], 0, v[18:19]
	v_lshl_add_u64 v[130:131], s[14:15], 0, v[8:9]
	s_movk_i32 s14, 0x18b
	v_lshlrev_b32_e32 v8, 7, v11
	v_lshl_add_u64 v[124:125], s[22:23], 0, v[16:17]
	v_cmp_lt_u32_e64 s[48:49], s14, v7
	s_movk_i32 s14, 0x197
	v_lshl_add_u64 v[8:9], s[4:5], 0, v[8:9]
	v_lshlrev_b32_e32 v16, 1, v13
	s_add_u32 s36, s4, 4.0
	v_cmp_lt_u32_e64 s[50:51], s14, v7
	v_lshl_add_u64 v[8:9], v[8:9], 0, v[16:17]
	s_mov_b64 s[14:15], 0x1e800000
	s_addc_u32 s37, s5, 0
	v_lshl_add_u64 v[132:133], v[8:9], 0, s[14:15]
	v_lshl_add_u64 v[136:137], s[4:5], 0, v[34:35]
	s_lshl_b32 s14, s26, 4
	v_readlane_b32 s4, v252, 13
	v_add_u32_e32 v14, v3, v4
	v_lshlrev_b32_e32 v2, 11, v2
	s_add_i32 s38, s4, s14
	v_mov_b32_e32 v3, 0x20000
	s_mov_b32 s4, 0x3c000
	v_bitop3_b32 v152, v2, s4, v3 bitop3:0xc8
	s_mov_b64 s[4:5], 0x30800000
	v_lshl_add_u64 v[138:139], v[136:137], 0, s[4:5]
	v_readlane_b32 s4, v252, 14
	v_lshlrev_b32_e32 v6, 3, v5
	v_lshlrev_b32_e64 v1, v11, 2
	s_mov_b64 s[6:7], 0x22800000
	v_and_b32_e32 v151, 0x1c000, v2
	s_add_i32 s4, s4, s14
	v_lshlrev_b32_e32 v104, 3, v7
	v_add_u32_e32 v149, -1, v1
	v_add_u32_e32 v150, -1, v105
	v_lshl_add_u64 v[134:135], v[8:9], 0, s[6:7]
	s_lshl_b32 s39, s27, 7
	v_or_b32_e32 v153, 0x20000, v151
	v_sub_u32_e32 v154, s4, v105
	v_sub_u32_e32 v155, s4, v1
	v_lshlrev_b32_e32 v156, 1, v6
	v_lshlrev_b32_e32 v157, 1, v10
	v_lshlrev_b32_e32 v158, 1, v12
	v_lshlrev_b32_e32 v159, 1, v14
	v_lshlrev_b32_e32 v160, 1, v4
	s_branch .LBB0_196

.LBB0_551:
	s_or_b64 exec, exec, s[18:19]
	v_mov_b32_e32 v36, v0
	s_waitcnt lgkmcnt(0)
	s_barrier
	s_mov_b32 s23, s93
	v_readfirstlane_b32 s4, v36
	s_ashr_i32 s22, s4, 6
	v_readlane_b32 s4, v253, 62
	s_add_i32 s34, s22, s4
	s_mov_b64 s[4:5], s[62:63]
	s_mov_b32 s20, 13
	s_mov_b32 s14, 14
	s_cmpk_gt_i32 s34, 0x1fff
	s_cbranch_scc1 .LBB0_554
	s_lshl_b32 s35, s23, 3
	s_add_u32 s18, s4, 0xc800000
	s_addc_u32 s19, s5, 0
	s_ashr_i32 s21, s20, 31
	s_lshl_b64 s[16:17], s[20:21], 3
	s_add_u32 s16, s84, s16
	s_addc_u32 s17, s85, s17
	s_add_u32 s36, s4, 0x4f500000
	s_addc_u32 s37, s5, 0
	s_ashr_i32 s15, s14, 31
	s_lshl_b64 s[14:15], s[14:15], 3
	s_add_u32 s14, s84, s14
	s_addc_u32 s15, s85, s15
	s_load_dwordx2 s[14:15], s[14:15], 0x0
	v_readlane_b32 s6, v252, 37
	s_load_dwordx2 s[16:17], s[16:17], 0x0
	v_readlane_b32 s7, v252, 38
	s_lshl_b64 s[20:21], s[6:7], 2
	s_waitcnt lgkmcnt(0)
	s_add_u32 s14, s14, s20
	s_addc_u32 s15, s15, s21
	v_and_b32_e32 v34, 63, v36
	s_add_u32 s16, s16, s20
	v_lshlrev_b32_e32 v1, 5, v34
	s_addc_u32 s17, s17, s21
	global_load_dwordx4 v[2:5], v1, s[14:15] offset:2048 nt
	global_load_dwordx4 v[6:9], v1, s[14:15] offset:2064 nt
	global_load_dwordx4 v[10:13], v1, s[16:17] offset:2048 nt
	global_load_dwordx4 v[14:17], v1, s[16:17] offset:2064 nt
	global_load_dwordx4 v[18:21], v1, s[14:15] nt
	global_load_dwordx4 v[22:25], v1, s[14:15] offset:16 nt
	global_load_dwordx4 v[26:29], v1, s[16:17] nt
	global_load_dwordx4 v[30:33], v1, s[16:17] offset:16 nt
	s_add_u32 s16, s4, 0x1a800000
	s_addc_u32 s17, s5, 0
	s_add_u32 s20, s4, 0x30800000
	s_addc_u32 s21, s5, 0
	s_add_u32 s4, s4, 0x1e800000
	v_lshlrev_b32_e32 v34, 4, v34
	s_addc_u32 s5, s5, 0
	v_and_b32_e32 v140, 0x70, v34
	v_lshl_add_u64 v[142:143], s[4:5], 0, v[34:35]
	v_or_b32_e32 v34, 0x400, v34
	v_lshlrev_b32_e32 v1, 6, v36
	v_lshl_add_u64 v[144:145], s[4:5], 0, v[34:35]
	s_lshl_b32 s4, s22, 2
	v_readlane_b32 s5, v252, 15
	v_and_b32_e32 v1, 0x1c0, v1
	v_bfe_u32 v141, v36, 3, 3
	s_add_i32 s22, s5, s4
	s_lshl_b32 s4, s23, 5
.LBB0_553:
	s_ashr_i32 s14, s34, 8
	v_and_or_b32 v36, s14, -16, v141
	v_ashrrev_i32_e32 v37, 31, v36
	s_and_b32 s5, s22, 0x3ffc
	v_lshlrev_b64 v[38:39], 21, v[36:37]
	v_lshl_or_b32 v34, s5, 7, v1
	v_lshl_add_u64 v[38:39], s[16:17], 0, v[38:39]
	v_lshl_add_u64 v[38:39], v[38:39], 0, v[34:35]
	global_load_dwordx4 v[88:91], v[38:39], off nt
	global_load_dwordx4 v[92:95], v[38:39], off offset:16 nt
	global_load_dwordx4 v[96:99], v[38:39], off offset:32 nt
	global_load_dwordx4 v[100:103], v[38:39], off offset:48 nt
	v_lshl_or_b32 v38, v36, 14, s5
	v_ashrrev_i32_e32 v39, 31, v38
	v_lshlrev_b64 v[42:43], 7, v[38:39]
	s_lshl_b32 s15, s5, 2
	v_or_b32_e32 v42, v42, v140
	s_add_u32 s24, s36, s15
	v_lshl_add_u64 v[44:45], s[20:21], 0, v[42:43]
	s_addc_u32 s25, s37, 0
	v_lshlrev_b64 v[40:41], 16, v[36:37]
	global_load_dwordx4 v[132:135], v[44:45], off nt
	v_lshl_add_u64 v[42:43], s[18:19], 0, v[42:43]
	v_lshl_add_u64 v[40:41], s[24:25], 0, v[40:41]
	global_load_dwordx4 v[136:139], v[42:43], off nt
	flat_load_dwordx4 v[104:107], v[40:41] nt
	v_or_b32_e32 v40, 1, v38
	v_ashrrev_i32_e32 v41, 31, v40
	v_lshlrev_b64 v[40:41], 7, v[40:41]
	v_or_b32_e32 v40, v40, v140
	v_lshl_add_u64 v[42:43], s[20:21], 0, v[40:41]
	v_lshl_add_u64 v[40:41], s[18:19], 0, v[40:41]
	global_load_dwordx4 v[124:127], v[42:43], off nt
	global_load_dwordx4 v[128:131], v[40:41], off nt
	v_or_b32_e32 v40, 2, v38
	v_ashrrev_i32_e32 v41, 31, v40
	v_lshlrev_b64 v[40:41], 7, v[40:41]
	v_or_b32_e32 v52, 8, v36
	v_or_b32_e32 v40, v40, v140
	v_ashrrev_i32_e32 v53, 31, v52
	v_lshl_add_u64 v[42:43], s[20:21], 0, v[40:41]
	v_lshl_add_u64 v[40:41], s[18:19], 0, v[40:41]
	v_lshlrev_b64 v[36:37], 21, v[52:53]
	global_load_dwordx4 v[116:119], v[42:43], off nt
	global_load_dwordx4 v[120:123], v[40:41], off nt
	v_lshl_add_u64 v[36:37], s[16:17], 0, v[36:37]
	v_lshl_add_u64 v[48:49], v[36:37], 0, v[34:35]
	v_or_b32_e32 v38, 3, v38
	v_ashrrev_i32_e32 v39, 31, v38
	v_lshlrev_b64 v[38:39], 7, v[38:39]
	v_or_b32_e32 v38, v38, v140
	v_lshl_add_u64 v[40:41], s[20:21], 0, v[38:39]
	v_lshl_add_u64 v[38:39], s[18:19], 0, v[38:39]
	global_load_dwordx4 v[108:111], v[40:41], off nt
	global_load_dwordx4 v[112:115], v[38:39], off nt
	v_lshl_or_b32 v56, v52, 14, s5
	v_ashrrev_i32_e32 v57, 31, v56
	v_lshlrev_b64 v[54:55], 7, v[56:57]
	v_or_b32_e32 v54, v54, v140
	v_lshl_add_u64 v[58:59], s[20:21], 0, v[54:55]
	global_load_dwordx4 v[36:39], v[48:49], off nt
	global_load_dwordx4 v[40:43], v[48:49], off offset:16 nt
	global_load_dwordx4 v[44:47], v[48:49], off offset:32 nt
	s_nop 0
	global_load_dwordx4 v[48:51], v[48:49], off offset:48 nt
	v_lshlrev_b64 v[52:53], 16, v[52:53]
	global_load_dwordx4 v[80:83], v[58:59], off nt
	v_or_b32_e32 v58, 1, v56
	v_ashrrev_i32_e32 v59, 31, v58
	v_lshlrev_b64 v[58:59], 7, v[58:59]
	v_or_b32_e32 v58, v58, v140
	v_lshl_add_u64 v[52:53], s[24:25], 0, v[52:53]
	v_lshl_add_u64 v[54:55], s[18:19], 0, v[54:55]
	v_lshl_add_u64 v[60:61], s[20:21], 0, v[58:59]
	v_lshl_add_u64 v[58:59], s[18:19], 0, v[58:59]
	global_load_dwordx4 v[84:87], v[54:55], off nt
	s_nop 0
	flat_load_dwordx4 v[52:55], v[52:53] nt
	s_ashr_i32 s23, s22, 31
	global_load_dwordx4 v[72:75], v[60:61], off nt
	global_load_dwordx4 v[76:79], v[58:59], off nt
	v_or_b32_e32 v58, 2, v56
	v_ashrrev_i32_e32 v59, 31, v58
	v_lshlrev_b64 v[58:59], 7, v[58:59]
	v_or_b32_e32 v58, v58, v140
	v_or_b32_e32 v56, 3, v56
	v_lshl_add_u64 v[60:61], s[20:21], 0, v[58:59]
	v_lshl_add_u64 v[58:59], s[18:19], 0, v[58:59]
	v_ashrrev_i32_e32 v57, 31, v56
	global_load_dwordx4 v[64:67], v[60:61], off nt
	global_load_dwordx4 v[68:71], v[58:59], off nt
	v_lshlrev_b64 v[60:61], 7, v[56:57]
	v_or_b32_e32 v60, v60, v140
	s_lshl_b64 s[24:25], s[22:23], 11
	v_lshl_add_u64 v[56:57], s[20:21], 0, v[60:61]
	s_waitcnt vmcnt(0)
	v_lshlrev_b32_e32 v160, 16, v88
	v_lshlrev_b32_e32 v161, 16, v90
	v_add_f32_e32 v34, 0, v160
	v_add_f32_e32 v34, v34, v161
	v_lshlrev_b32_e32 v152, 16, v96
	v_lshlrev_b32_e32 v153, 16, v98
	v_lshlrev_b32_e32 v146, 16, v100
	v_lshlrev_b32_e32 v147, 16, v102
	v_lshl_add_u64 v[60:61], s[18:19], 0, v[60:61]
	global_load_dwordx4 v[56:59], v[56:57], off nt
	s_add_i32 s14, s22, 1
	global_load_dwordx4 v[60:63], v[60:61], off nt
	s_ashr_i32 s15, s14, 31
	v_cvt_f32_f16_e32 v148, v135
	v_cvt_f32_f16_sdwa v149, v135 dst_sel:DWORD dst_unused:UNUSED_PAD src0_sel:WORD_1
	v_cvt_f32_f16_e32 v154, v134
	v_cvt_f32_f16_sdwa v155, v134 dst_sel:DWORD dst_unused:UNUSED_PAD src0_sel:WORD_1
	v_cvt_f32_f16_e32 v134, v138
	v_cvt_f32_f16_sdwa v135, v138 dst_sel:DWORD dst_unused:UNUSED_PAD src0_sel:WORD_1
	v_lshlrev_b32_e32 v138, 16, v92
	v_cvt_f32_f16_e32 v150, v139
	v_cvt_f32_f16_sdwa v151, v139 dst_sel:DWORD dst_unused:UNUSED_PAD src0_sel:WORD_1
	v_lshlrev_b32_e32 v139, 16, v94
	v_add_f32_e32 v34, v34, v138
	v_add_f32_e32 v34, v34, v139
	v_add_f32_e32 v34, v34, v152
	v_add_f32_e32 v34, v34, v153
	v_add_f32_e32 v34, v34, v146
	v_add_f32_e32 v34, v34, v147
	v_cvt_f32_f16_e32 v156, v133
	v_cvt_f32_f16_sdwa v157, v133 dst_sel:DWORD dst_unused:UNUSED_PAD src0_sel:WORD_1
	v_add_f32_dpp v34, v34, v34 quad_perm:[1,0,3,2] row_mask:0xf bank_mask:0xf bound_ctrl:1
	v_cvt_f32_f16_e32 v158, v137
	v_cvt_f32_f16_sdwa v159, v137 dst_sel:DWORD dst_unused:UNUSED_PAD src0_sel:WORD_1
	v_add_f32_dpp v34, v34, v34 quad_perm:[2,3,0,1] row_mask:0xf bank_mask:0xf bound_ctrl:1
	v_cvt_f32_f16_e32 v162, v132
	v_cvt_f32_f16_sdwa v163, v132 dst_sel:DWORD dst_unused:UNUSED_PAD src0_sel:WORD_1
	v_add_f32_dpp v34, v34, v34 row_half_mirror row_mask:0xf bank_mask:0xf bound_ctrl:1
	v_mul_f32_e32 v34, 0x3c800000, v34
	v_cvt_f32_f16_e32 v132, v136
	v_cvt_f32_f16_sdwa v133, v136 dst_sel:DWORD dst_unused:UNUSED_PAD src0_sel:WORD_1
	v_pk_add_f32 v[136:137], v[160:161], v[34:35] op_sel_hi:[1,0] neg_lo:[0,1] neg_hi:[0,1]
	v_pk_add_f32 v[138:139], v[138:139], v[34:35] op_sel_hi:[1,0] neg_lo:[0,1] neg_hi:[0,1]
	v_pk_mul_f32 v[160:161], v[136:137], v[136:137]
	v_pk_mul_f32 v[164:165], v[138:139], v[138:139]
	v_pk_add_f32 v[152:153], v[152:153], v[34:35] op_sel_hi:[1,0] neg_lo:[0,1] neg_hi:[0,1]
	v_pk_add_f32 v[146:147], v[146:147], v[34:35] op_sel_hi:[1,0] neg_lo:[0,1] neg_hi:[0,1]
	v_add_f32_e32 v34, v160, v161
	v_add_f32_e32 v34, v164, v34
	v_pk_mul_f32 v[166:167], v[152:153], v[152:153]
	v_add_f32_e32 v34, v165, v34
	v_add_f32_e32 v34, v166, v34
	v_pk_mul_f32 v[168:169], v[146:147], v[146:147]
	v_add_f32_e32 v34, v167, v34
	v_add_f32_e32 v34, v168, v34
	v_add_f32_e32 v34, v169, v34
	s_lshl_b64 s[26:27], s[14:15], 11
	s_add_i32 s14, s22, 2
	v_add_f32_dpp v34, v34, v34 quad_perm:[1,0,3,2] row_mask:0xf bank_mask:0xf bound_ctrl:1
	s_ashr_i32 s15, s14, 31
	s_lshl_b64 s[28:29], s[14:15], 11
	v_add_f32_dpp v34, v34, v34 quad_perm:[2,3,0,1] row_mask:0xf bank_mask:0xf bound_ctrl:1
	s_add_i32 s14, s22, 3
	s_ashr_i32 s15, s14, 31
	v_add_f32_dpp v34, v34, v34 row_half_mirror row_mask:0xf bank_mask:0xf bound_ctrl:1
	v_fmamk_f32 v34, v34, 0x3c800000, v216
	v_rsq_f32_e32 v34, v34
	s_lshl_b64 s[30:31], s[14:15], 11
	s_add_i32 s34, s34, s35
	s_add_i32 s22, s22, s4
	v_pk_mul_f32 v[136:137], v[136:137], v[34:35] op_sel_hi:[1,0]
	s_cmpk_lt_i32 s34, 0x2000
	v_pk_fma_f32 v[136:137], v[26:27], v[136:137], v[18:19]
	s_waitcnt lgkmcnt(0)
	v_pk_fma_f32 v[136:137], v[104:105], v[162:163], v[136:137] op_sel_hi:[0,1,1]
	v_pk_mul_f32 v[132:133], v[136:137], v[132:133]
	v_pk_mul_f32 v[136:137], v[138:139], v[34:35] op_sel_hi:[1,0]
	v_pk_mul_f32 v[138:139], v[152:153], v[34:35] op_sel_hi:[1,0]
	v_pk_fma_f32 v[136:137], v[28:29], v[136:137], v[20:21]
	v_pk_fma_f32 v[138:139], v[30:31], v[138:139], v[22:23]
	v_pk_fma_f32 v[136:137], v[104:105], v[156:157], v[136:137] op_sel_hi:[0,1,1]
	v_pk_fma_f32 v[138:139], v[104:105], v[154:155], v[138:139] op_sel_hi:[0,1,1]
	v_pk_mul_f32 v[134:135], v[138:139], v[134:135]
	v_pk_mul_f32 v[138:139], v[146:147], v[34:35] op_sel_hi:[1,0]
	v_pk_mul_f32 v[136:137], v[136:137], v[158:159]
	v_pk_fma_f32 v[138:139], v[32:33], v[138:139], v[24:25]
	v_and_b32_e32 v152, 0xffff0000, v88
	v_pk_fma_f32 v[138:139], v[104:105], v[148:149], v[138:139] op_sel_hi:[0,1,1]
	v_pk_mul_f32 v[138:139], v[138:139], v[150:151]
	v_cvt_pk_bf16_f32 v132, v132, v133
	v_cvt_pk_bf16_f32 v133, v136, v137
	v_cvt_pk_bf16_f32 v134, v134, v135
	v_cvt_pk_bf16_f32 v135, v138, v139
	v_lshl_add_u64 v[136:137], v[142:143], 0, s[24:25]
	v_and_b32_e32 v153, 0xffff0000, v90
	v_add_f32_e32 v34, 0, v152
	global_store_dwordx4 v[136:137], v[132:135], off
	v_cvt_f32_f16_e32 v146, v126
	v_cvt_f32_f16_sdwa v147, v126 dst_sel:DWORD dst_unused:UNUSED_PAD src0_sel:WORD_1
	v_cvt_f32_f16_e32 v134, v127
	v_cvt_f32_f16_sdwa v135, v127 dst_sel:DWORD dst_unused:UNUSED_PAD src0_sel:WORD_1
	v_cvt_f32_f16_e32 v126, v130
	v_cvt_f32_f16_sdwa v127, v130 dst_sel:DWORD dst_unused:UNUSED_PAD src0_sel:WORD_1
	v_and_b32_e32 v130, 0xffff0000, v92
	v_add_f32_e32 v34, v34, v153
	v_cvt_f32_f16_e32 v136, v131
	v_cvt_f32_f16_sdwa v137, v131 dst_sel:DWORD dst_unused:UNUSED_PAD src0_sel:WORD_1
	v_and_b32_e32 v131, 0xffff0000, v94
	v_add_f32_e32 v34, v34, v130
	v_and_b32_e32 v138, 0xffff0000, v96
	v_add_f32_e32 v34, v34, v131
	v_and_b32_e32 v139, 0xffff0000, v98
	v_add_f32_e32 v34, v34, v138
	v_and_b32_e32 v132, 0xffff0000, v100
	v_add_f32_e32 v34, v34, v139
	v_and_b32_e32 v133, 0xffff0000, v102
	v_add_f32_e32 v34, v34, v132
	v_add_f32_e32 v34, v34, v133
	v_cvt_f32_f16_e32 v148, v125
	v_cvt_f32_f16_sdwa v149, v125 dst_sel:DWORD dst_unused:UNUSED_PAD src0_sel:WORD_1
	v_add_f32_dpp v34, v34, v34 quad_perm:[1,0,3,2] row_mask:0xf bank_mask:0xf bound_ctrl:1
	v_cvt_f32_f16_e32 v150, v129
	v_cvt_f32_f16_sdwa v151, v129 dst_sel:DWORD dst_unused:UNUSED_PAD src0_sel:WORD_1
	v_add_f32_dpp v34, v34, v34 quad_perm:[2,3,0,1] row_mask:0xf bank_mask:0xf bound_ctrl:1
	v_cvt_f32_f16_e32 v154, v124
	v_cvt_f32_f16_sdwa v155, v124 dst_sel:DWORD dst_unused:UNUSED_PAD src0_sel:WORD_1
	v_add_f32_dpp v34, v34, v34 row_half_mirror row_mask:0xf bank_mask:0xf bound_ctrl:1
	v_mul_f32_e32 v34, 0x3c800000, v34
	v_cvt_f32_f16_e32 v124, v128
	v_cvt_f32_f16_sdwa v125, v128 dst_sel:DWORD dst_unused:UNUSED_PAD src0_sel:WORD_1
	v_pk_add_f32 v[128:129], v[152:153], v[34:35] op_sel_hi:[1,0] neg_lo:[0,1] neg_hi:[0,1]
	v_pk_add_f32 v[130:131], v[130:131], v[34:35] op_sel_hi:[1,0] neg_lo:[0,1] neg_hi:[0,1]
	v_pk_mul_f32 v[152:153], v[128:129], v[128:129]
	v_pk_mul_f32 v[156:157], v[130:131], v[130:131]
	v_pk_add_f32 v[138:139], v[138:139], v[34:35] op_sel_hi:[1,0] neg_lo:[0,1] neg_hi:[0,1]
	v_pk_add_f32 v[132:133], v[132:133], v[34:35] op_sel_hi:[1,0] neg_lo:[0,1] neg_hi:[0,1]
	v_add_f32_e32 v34, v152, v153
	v_add_f32_e32 v34, v156, v34
	v_pk_mul_f32 v[158:159], v[138:139], v[138:139]
	v_add_f32_e32 v34, v157, v34
	v_add_f32_e32 v34, v158, v34
	v_pk_mul_f32 v[160:161], v[132:133], v[132:133]
	v_add_f32_e32 v34, v159, v34
	v_add_f32_e32 v34, v160, v34
	v_add_f32_e32 v34, v161, v34
	v_and_b32_e32 v90, 0xffff0000, v89
	v_and_b32_e32 v94, 0xffff0000, v93
	v_add_f32_dpp v34, v34, v34 quad_perm:[1,0,3,2] row_mask:0xf bank_mask:0xf bound_ctrl:1
	v_cvt_f32_f16_e32 v92, v109
	v_cvt_f32_f16_e32 v88, v108
	v_add_f32_dpp v34, v34, v34 quad_perm:[2,3,0,1] row_mask:0xf bank_mask:0xf bound_ctrl:1
	v_and_b32_e32 v98, 0xffff0000, v97
	v_and_b32_e32 v102, 0xffff0000, v101
	v_add_f32_dpp v34, v34, v34 row_half_mirror row_mask:0xf bank_mask:0xf bound_ctrl:1
	v_fmamk_f32 v34, v34, 0x3c800000, v216
	v_rsq_f32_e32 v34, v34
	v_cvt_f32_f16_e32 v100, v111
	v_cvt_f32_f16_e32 v96, v110
	v_pk_mul_f32 v[128:129], v[128:129], v[34:35] op_sel_hi:[1,0]
	s_nop 0
	v_pk_fma_f32 v[128:129], v[26:27], v[128:129], v[18:19]
	s_nop 0
	v_pk_fma_f32 v[128:129], v[104:105], v[154:155], v[128:129] op_sel:[1,0,0]
	s_nop 0
	v_pk_mul_f32 v[124:125], v[128:129], v[124:125]
	v_pk_mul_f32 v[128:129], v[130:131], v[34:35] op_sel_hi:[1,0]
	v_pk_mul_f32 v[130:131], v[138:139], v[34:35] op_sel_hi:[1,0]
	v_pk_fma_f32 v[128:129], v[28:29], v[128:129], v[20:21]
	v_pk_fma_f32 v[130:131], v[30:31], v[130:131], v[22:23]
	v_pk_fma_f32 v[128:129], v[104:105], v[148:149], v[128:129] op_sel:[1,0,0]
	v_pk_fma_f32 v[130:131], v[104:105], v[146:147], v[130:131] op_sel:[1,0,0]
	v_pk_mul_f32 v[128:129], v[128:129], v[150:151]
	v_pk_mul_f32 v[126:127], v[130:131], v[126:127]
	v_pk_mul_f32 v[130:131], v[132:133], v[34:35] op_sel_hi:[1,0]
	v_cvt_pk_bf16_f32 v124, v124, v125
	v_pk_fma_f32 v[130:131], v[32:33], v[130:131], v[24:25]
	v_cvt_pk_bf16_f32 v125, v128, v129
	v_pk_fma_f32 v[104:105], v[104:105], v[134:135], v[130:131] op_sel:[1,0,0]
	v_cvt_pk_bf16_f32 v126, v126, v127
	v_pk_mul_f32 v[104:105], v[104:105], v[136:137]
	v_lshlrev_b32_e32 v136, 16, v89
	v_cvt_pk_bf16_f32 v127, v104, v105
	v_lshl_add_u64 v[104:105], v[142:143], 0, s[26:27]
	v_lshlrev_b32_e32 v137, 16, v91
	v_add_f32_e32 v34, 0, v136
	global_store_dwordx4 v[104:105], v[124:127], off
	v_cvt_f32_f16_e32 v130, v118
	v_cvt_f32_f16_sdwa v131, v118 dst_sel:DWORD dst_unused:UNUSED_PAD src0_sel:WORD_1
	v_cvt_f32_f16_e32 v124, v119
	v_cvt_f32_f16_sdwa v125, v119 dst_sel:DWORD dst_unused:UNUSED_PAD src0_sel:WORD_1
	v_cvt_f32_f16_e32 v118, v122
	v_cvt_f32_f16_sdwa v119, v122 dst_sel:DWORD dst_unused:UNUSED_PAD src0_sel:WORD_1
	v_lshlrev_b32_e32 v122, 16, v93
	v_add_f32_e32 v34, v34, v137
	v_cvt_f32_f16_e32 v126, v123
	v_cvt_f32_f16_sdwa v127, v123 dst_sel:DWORD dst_unused:UNUSED_PAD src0_sel:WORD_1
	v_lshlrev_b32_e32 v123, 16, v95
	v_add_f32_e32 v34, v34, v122
	v_lshlrev_b32_e32 v128, 16, v97
	v_add_f32_e32 v34, v34, v123
	v_lshlrev_b32_e32 v129, 16, v99
	v_add_f32_e32 v34, v34, v128
	v_lshlrev_b32_e32 v104, 16, v101
	v_add_f32_e32 v34, v34, v129
	v_lshlrev_b32_e32 v105, 16, v103
	v_add_f32_e32 v34, v34, v104
	v_add_f32_e32 v34, v34, v105
	v_cvt_f32_f16_e32 v132, v117
	v_cvt_f32_f16_sdwa v133, v117 dst_sel:DWORD dst_unused:UNUSED_PAD src0_sel:WORD_1
	v_add_f32_dpp v34, v34, v34 quad_perm:[1,0,3,2] row_mask:0xf bank_mask:0xf bound_ctrl:1
	v_cvt_f32_f16_e32 v134, v121
	v_cvt_f32_f16_sdwa v135, v121 dst_sel:DWORD dst_unused:UNUSED_PAD src0_sel:WORD_1
	v_add_f32_dpp v34, v34, v34 quad_perm:[2,3,0,1] row_mask:0xf bank_mask:0xf bound_ctrl:1
	v_cvt_f32_f16_e32 v138, v116
	v_cvt_f32_f16_sdwa v139, v116 dst_sel:DWORD dst_unused:UNUSED_PAD src0_sel:WORD_1
	v_add_f32_dpp v34, v34, v34 row_half_mirror row_mask:0xf bank_mask:0xf bound_ctrl:1
	v_mul_f32_e32 v34, 0x3c800000, v34
	v_cvt_f32_f16_e32 v116, v120
	v_cvt_f32_f16_sdwa v117, v120 dst_sel:DWORD dst_unused:UNUSED_PAD src0_sel:WORD_1
	v_pk_add_f32 v[120:121], v[136:137], v[34:35] op_sel_hi:[1,0] neg_lo:[0,1] neg_hi:[0,1]
	v_pk_add_f32 v[122:123], v[122:123], v[34:35] op_sel_hi:[1,0] neg_lo:[0,1] neg_hi:[0,1]
	v_pk_mul_f32 v[136:137], v[120:121], v[120:121]
	v_pk_mul_f32 v[146:147], v[122:123], v[122:123]
	v_pk_add_f32 v[128:129], v[128:129], v[34:35] op_sel_hi:[1,0] neg_lo:[0,1] neg_hi:[0,1]
	v_pk_add_f32 v[104:105], v[104:105], v[34:35] op_sel_hi:[1,0] neg_lo:[0,1] neg_hi:[0,1]
	v_add_f32_e32 v34, v136, v137
	v_add_f32_e32 v34, v146, v34
	v_pk_mul_f32 v[148:149], v[128:129], v[128:129]
	v_add_f32_e32 v34, v147, v34
	v_add_f32_e32 v34, v148, v34
	v_pk_mul_f32 v[150:151], v[104:105], v[104:105]
	v_add_f32_e32 v34, v149, v34
	v_add_f32_e32 v34, v150, v34
	v_add_f32_e32 v34, v151, v34
	v_cvt_f32_f16_sdwa v93, v109 dst_sel:DWORD dst_unused:UNUSED_PAD src0_sel:WORD_1
	v_and_b32_e32 v91, 0xffff0000, v91
	v_add_f32_dpp v34, v34, v34 quad_perm:[1,0,3,2] row_mask:0xf bank_mask:0xf bound_ctrl:1
	v_cvt_f32_f16_sdwa v89, v108 dst_sel:DWORD dst_unused:UNUSED_PAD src0_sel:WORD_1
	v_cvt_f32_f16_e32 v108, v112
	v_add_f32_dpp v34, v34, v34 quad_perm:[2,3,0,1] row_mask:0xf bank_mask:0xf bound_ctrl:1
	v_cvt_f32_f16_sdwa v109, v112 dst_sel:DWORD dst_unused:UNUSED_PAD src0_sel:WORD_1
	v_add_f32_e32 v112, 0, v90
	v_add_f32_dpp v34, v34, v34 row_half_mirror row_mask:0xf bank_mask:0xf bound_ctrl:1
	v_fmamk_f32 v34, v34, 0x3c800000, v216
	v_rsq_f32_e32 v34, v34
	v_add_f32_e32 v112, v112, v91
	v_and_b32_e32 v95, 0xffff0000, v95
	v_add_f32_e32 v112, v112, v94
	v_add_f32_e32 v112, v112, v95
	v_and_b32_e32 v99, 0xffff0000, v99
	v_add_f32_e32 v112, v112, v98
	v_pk_mul_f32 v[120:121], v[120:121], v[34:35] op_sel_hi:[1,0]
	v_add_f32_e32 v112, v112, v99
	v_pk_fma_f32 v[120:121], v[26:27], v[120:121], v[18:19]
	v_and_b32_e32 v103, 0xffff0000, v103
	v_add_f32_e32 v112, v112, v102
	v_pk_fma_f32 v[120:121], v[106:107], v[138:139], v[120:121] op_sel_hi:[0,1,1]
	v_add_f32_e32 v112, v112, v103
	v_pk_mul_f32 v[116:117], v[120:121], v[116:117]
	v_pk_mul_f32 v[120:121], v[122:123], v[34:35] op_sel_hi:[1,0]
	v_pk_mul_f32 v[122:123], v[128:129], v[34:35] op_sel_hi:[1,0]
	v_pk_mul_f32 v[104:105], v[104:105], v[34:35] op_sel_hi:[1,0]
	v_add_f32_dpp v112, v112, v112 quad_perm:[1,0,3,2] row_mask:0xf bank_mask:0xf bound_ctrl:1
	v_pk_fma_f32 v[120:121], v[28:29], v[120:121], v[20:21]
	v_pk_fma_f32 v[122:123], v[30:31], v[122:123], v[22:23]
	v_pk_fma_f32 v[104:105], v[32:33], v[104:105], v[24:25]
	v_add_f32_dpp v112, v112, v112 quad_perm:[2,3,0,1] row_mask:0xf bank_mask:0xf bound_ctrl:1
	v_pk_fma_f32 v[120:121], v[106:107], v[132:133], v[120:121] op_sel_hi:[0,1,1]
	v_pk_fma_f32 v[122:123], v[106:107], v[130:131], v[122:123] op_sel_hi:[0,1,1]
	v_pk_fma_f32 v[104:105], v[106:107], v[124:125], v[104:105] op_sel_hi:[0,1,1]
	v_add_f32_dpp v112, v112, v112 row_half_mirror row_mask:0xf bank_mask:0xf bound_ctrl:1
	v_pk_mul_f32 v[120:121], v[120:121], v[134:135]
	v_pk_mul_f32 v[118:119], v[122:123], v[118:119]
	v_pk_mul_f32 v[104:105], v[104:105], v[126:127]
	v_mul_f32_e32 v112, 0x3c800000, v112
	v_cvt_pk_bf16_f32 v116, v116, v117
	v_cvt_pk_bf16_f32 v117, v120, v121
	v_cvt_pk_bf16_f32 v118, v118, v119
	v_cvt_pk_bf16_f32 v119, v104, v105
	v_lshl_add_u64 v[104:105], v[142:143], 0, s[28:29]
	v_pk_add_f32 v[90:91], v[90:91], v[112:113] op_sel_hi:[1,0] neg_lo:[0,1] neg_hi:[0,1]
	global_store_dwordx4 v[104:105], v[116:119], off
	v_cvt_f32_f16_sdwa v101, v111 dst_sel:DWORD dst_unused:UNUSED_PAD src0_sel:WORD_1
	v_cvt_f32_f16_e32 v104, v115
	v_cvt_f32_f16_sdwa v105, v115 dst_sel:DWORD dst_unused:UNUSED_PAD src0_sel:WORD_1
	v_cvt_f32_f16_sdwa v97, v110 dst_sel:DWORD dst_unused:UNUSED_PAD src0_sel:WORD_1
	v_cvt_f32_f16_e32 v110, v114
	v_cvt_f32_f16_sdwa v111, v114 dst_sel:DWORD dst_unused:UNUSED_PAD src0_sel:WORD_1
	v_pk_mul_f32 v[114:115], v[90:91], v[90:91]
	v_pk_add_f32 v[94:95], v[94:95], v[112:113] op_sel_hi:[1,0] neg_lo:[0,1] neg_hi:[0,1]
	v_add_f32_e32 v114, v114, v115
	v_pk_mul_f32 v[116:117], v[94:95], v[94:95]
	v_pk_add_f32 v[98:99], v[98:99], v[112:113] op_sel_hi:[1,0] neg_lo:[0,1] neg_hi:[0,1]
	v_add_f32_e32 v114, v116, v114
	v_pk_mul_f32 v[118:119], v[98:99], v[98:99]
	v_add_f32_e32 v114, v117, v114
	v_pk_add_f32 v[102:103], v[102:103], v[112:113] op_sel_hi:[1,0] neg_lo:[0,1] neg_hi:[0,1]
	v_add_f32_e32 v114, v118, v114
	v_mov_b32_e32 v34, v107
	v_cvt_f32_f16_e32 v106, v113
	v_cvt_f32_f16_sdwa v107, v113 dst_sel:DWORD dst_unused:UNUSED_PAD src0_sel:WORD_1
	v_pk_mul_f32 v[112:113], v[102:103], v[102:103]
	v_add_f32_e32 v114, v119, v114
	v_add_f32_e32 v112, v112, v114
	v_add_f32_e32 v112, v113, v112
	s_nop 1
	v_add_f32_dpp v112, v112, v112 quad_perm:[1,0,3,2] row_mask:0xf bank_mask:0xf bound_ctrl:1
	s_nop 1
	v_add_f32_dpp v112, v112, v112 quad_perm:[2,3,0,1] row_mask:0xf bank_mask:0xf bound_ctrl:1
	s_nop 1
	v_add_f32_dpp v112, v112, v112 row_half_mirror row_mask:0xf bank_mask:0xf bound_ctrl:1
	v_fmamk_f32 v112, v112, 0x3c800000, v216
	v_rsq_f32_e32 v112, v112
	s_nop 0
	v_pk_mul_f32 v[90:91], v[90:91], v[112:113] op_sel_hi:[1,0]
	s_nop 0
	v_pk_fma_f32 v[90:91], v[26:27], v[90:91], v[18:19]
	s_nop 0
	v_pk_fma_f32 v[88:89], v[34:35], v[88:89], v[90:91] op_sel_hi:[0,1,1]
	v_pk_mul_f32 v[90:91], v[94:95], v[112:113] op_sel_hi:[1,0]
	v_pk_mul_f32 v[94:95], v[102:103], v[112:113] op_sel_hi:[1,0]
	v_pk_fma_f32 v[90:91], v[28:29], v[90:91], v[20:21]
	v_pk_fma_f32 v[94:95], v[32:33], v[94:95], v[24:25]
	v_pk_fma_f32 v[90:91], v[34:35], v[92:93], v[90:91] op_sel_hi:[0,1,1]
	v_pk_mul_f32 v[92:93], v[98:99], v[112:113] op_sel_hi:[1,0]
	v_pk_fma_f32 v[94:95], v[34:35], v[100:101], v[94:95] op_sel_hi:[0,1,1]
	v_pk_fma_f32 v[92:93], v[30:31], v[92:93], v[22:23]
	v_pk_mul_f32 v[88:89], v[88:89], v[108:109]
	v_pk_fma_f32 v[92:93], v[34:35], v[96:97], v[92:93] op_sel_hi:[0,1,1]
	v_pk_mul_f32 v[90:91], v[90:91], v[106:107]
	v_pk_mul_f32 v[92:93], v[92:93], v[110:111]
	v_pk_mul_f32 v[94:95], v[94:95], v[104:105]
	v_lshlrev_b32_e32 v102, 16, v36
	v_cvt_pk_bf16_f32 v88, v88, v89
	v_cvt_pk_bf16_f32 v89, v90, v91
	v_cvt_pk_bf16_f32 v90, v92, v93
	v_cvt_pk_bf16_f32 v91, v94, v95
	v_lshl_add_u64 v[92:93], v[142:143], 0, s[30:31]
	v_lshlrev_b32_e32 v103, 16, v38
	v_add_f32_e32 v34, 0, v102
	global_store_dwordx4 v[92:93], v[88:91], off
	v_cvt_f32_f16_e32 v96, v82
	v_cvt_f32_f16_sdwa v97, v82 dst_sel:DWORD dst_unused:UNUSED_PAD src0_sel:WORD_1
	v_cvt_f32_f16_e32 v90, v83
	v_cvt_f32_f16_sdwa v91, v83 dst_sel:DWORD dst_unused:UNUSED_PAD src0_sel:WORD_1
	v_cvt_f32_f16_e32 v82, v86
	v_cvt_f32_f16_sdwa v83, v86 dst_sel:DWORD dst_unused:UNUSED_PAD src0_sel:WORD_1
	v_lshlrev_b32_e32 v86, 16, v40
	v_add_f32_e32 v34, v34, v103
	v_cvt_f32_f16_e32 v92, v87
	v_cvt_f32_f16_sdwa v93, v87 dst_sel:DWORD dst_unused:UNUSED_PAD src0_sel:WORD_1
	v_lshlrev_b32_e32 v87, 16, v42
	v_add_f32_e32 v34, v34, v86
	v_lshlrev_b32_e32 v94, 16, v44
	v_add_f32_e32 v34, v34, v87
	v_lshlrev_b32_e32 v95, 16, v46
	v_add_f32_e32 v34, v34, v94
	v_lshlrev_b32_e32 v88, 16, v48
	v_add_f32_e32 v34, v34, v95
	v_lshlrev_b32_e32 v89, 16, v50
	v_add_f32_e32 v34, v34, v88
	v_add_f32_e32 v34, v34, v89
	v_cvt_f32_f16_e32 v98, v81
	v_cvt_f32_f16_sdwa v99, v81 dst_sel:DWORD dst_unused:UNUSED_PAD src0_sel:WORD_1
	v_add_f32_dpp v34, v34, v34 quad_perm:[1,0,3,2] row_mask:0xf bank_mask:0xf bound_ctrl:1
	v_cvt_f32_f16_e32 v100, v85
	v_cvt_f32_f16_sdwa v101, v85 dst_sel:DWORD dst_unused:UNUSED_PAD src0_sel:WORD_1
	v_add_f32_dpp v34, v34, v34 quad_perm:[2,3,0,1] row_mask:0xf bank_mask:0xf bound_ctrl:1
	v_cvt_f32_f16_e32 v104, v80
	v_cvt_f32_f16_sdwa v105, v80 dst_sel:DWORD dst_unused:UNUSED_PAD src0_sel:WORD_1
	v_add_f32_dpp v34, v34, v34 row_half_mirror row_mask:0xf bank_mask:0xf bound_ctrl:1
	v_mul_f32_e32 v34, 0x3c800000, v34
	v_cvt_f32_f16_e32 v80, v84
	v_cvt_f32_f16_sdwa v81, v84 dst_sel:DWORD dst_unused:UNUSED_PAD src0_sel:WORD_1
	v_pk_add_f32 v[84:85], v[102:103], v[34:35] op_sel_hi:[1,0] neg_lo:[0,1] neg_hi:[0,1]
	v_pk_add_f32 v[86:87], v[86:87], v[34:35] op_sel_hi:[1,0] neg_lo:[0,1] neg_hi:[0,1]
	v_pk_mul_f32 v[102:103], v[84:85], v[84:85]
	v_pk_mul_f32 v[106:107], v[86:87], v[86:87]
	v_pk_add_f32 v[94:95], v[94:95], v[34:35] op_sel_hi:[1,0] neg_lo:[0,1] neg_hi:[0,1]
	v_pk_add_f32 v[88:89], v[88:89], v[34:35] op_sel_hi:[1,0] neg_lo:[0,1] neg_hi:[0,1]
	v_add_f32_e32 v34, v102, v103
	v_add_f32_e32 v34, v106, v34
	v_pk_mul_f32 v[108:109], v[94:95], v[94:95]
	v_add_f32_e32 v34, v107, v34
	v_add_f32_e32 v34, v108, v34
	v_pk_mul_f32 v[110:111], v[88:89], v[88:89]
	v_add_f32_e32 v34, v109, v34
	v_add_f32_e32 v34, v110, v34
	v_add_f32_e32 v34, v111, v34
	s_nop 1
	v_add_f32_dpp v34, v34, v34 quad_perm:[1,0,3,2] row_mask:0xf bank_mask:0xf bound_ctrl:1
	s_nop 1
	v_add_f32_dpp v34, v34, v34 quad_perm:[2,3,0,1] row_mask:0xf bank_mask:0xf bound_ctrl:1
	s_nop 1
	v_add_f32_dpp v34, v34, v34 row_half_mirror row_mask:0xf bank_mask:0xf bound_ctrl:1
	v_fmamk_f32 v34, v34, 0x3c800000, v216
	v_rsq_f32_e32 v34, v34
	s_nop 0
	v_pk_mul_f32 v[84:85], v[84:85], v[34:35] op_sel_hi:[1,0]
	s_nop 0
	v_pk_fma_f32 v[84:85], v[10:11], v[84:85], v[2:3]
	s_nop 0
	v_pk_fma_f32 v[84:85], v[52:53], v[104:105], v[84:85] op_sel_hi:[0,1,1]
	v_pk_mul_f32 v[80:81], v[84:85], v[80:81]
	v_pk_mul_f32 v[84:85], v[86:87], v[34:35] op_sel_hi:[1,0]
	v_pk_mul_f32 v[86:87], v[94:95], v[34:35] op_sel_hi:[1,0]
	v_pk_fma_f32 v[84:85], v[12:13], v[84:85], v[4:5]
	v_pk_fma_f32 v[86:87], v[14:15], v[86:87], v[6:7]
	v_pk_fma_f32 v[84:85], v[52:53], v[98:99], v[84:85] op_sel_hi:[0,1,1]
	v_pk_fma_f32 v[86:87], v[52:53], v[96:97], v[86:87] op_sel_hi:[0,1,1]
	v_pk_mul_f32 v[82:83], v[86:87], v[82:83]
	v_pk_mul_f32 v[86:87], v[88:89], v[34:35] op_sel_hi:[1,0]
	v_pk_mul_f32 v[84:85], v[84:85], v[100:101]
	v_pk_fma_f32 v[86:87], v[16:17], v[86:87], v[8:9]
	v_and_b32_e32 v94, 0xffff0000, v36
	v_pk_fma_f32 v[86:87], v[52:53], v[90:91], v[86:87] op_sel_hi:[0,1,1]
	v_pk_mul_f32 v[86:87], v[86:87], v[92:93]
	v_cvt_pk_bf16_f32 v80, v80, v81
	v_cvt_pk_bf16_f32 v81, v84, v85
	v_cvt_pk_bf16_f32 v82, v82, v83
	v_cvt_pk_bf16_f32 v83, v86, v87
	v_lshl_add_u64 v[84:85], v[144:145], 0, s[24:25]
	v_and_b32_e32 v95, 0xffff0000, v38
	v_add_f32_e32 v34, 0, v94
	global_store_dwordx4 v[84:85], v[80:83], off
	v_cvt_f32_f16_e32 v88, v74
	v_cvt_f32_f16_sdwa v89, v74 dst_sel:DWORD dst_unused:UNUSED_PAD src0_sel:WORD_1
	v_cvt_f32_f16_e32 v82, v75
	v_cvt_f32_f16_sdwa v83, v75 dst_sel:DWORD dst_unused:UNUSED_PAD src0_sel:WORD_1
	v_cvt_f32_f16_e32 v74, v78
	v_cvt_f32_f16_sdwa v75, v78 dst_sel:DWORD dst_unused:UNUSED_PAD src0_sel:WORD_1
	v_and_b32_e32 v78, 0xffff0000, v40
	v_add_f32_e32 v34, v34, v95
	v_cvt_f32_f16_e32 v84, v79
	v_cvt_f32_f16_sdwa v85, v79 dst_sel:DWORD dst_unused:UNUSED_PAD src0_sel:WORD_1
	v_and_b32_e32 v79, 0xffff0000, v42
	v_add_f32_e32 v34, v34, v78
	v_and_b32_e32 v86, 0xffff0000, v44
	v_add_f32_e32 v34, v34, v79
	v_and_b32_e32 v87, 0xffff0000, v46
	v_add_f32_e32 v34, v34, v86
	v_and_b32_e32 v80, 0xffff0000, v48
	v_add_f32_e32 v34, v34, v87
	v_and_b32_e32 v81, 0xffff0000, v50
	v_add_f32_e32 v34, v34, v80
	v_add_f32_e32 v34, v34, v81
	v_cvt_f32_f16_e32 v90, v73
	v_cvt_f32_f16_sdwa v91, v73 dst_sel:DWORD dst_unused:UNUSED_PAD src0_sel:WORD_1
	v_add_f32_dpp v34, v34, v34 quad_perm:[1,0,3,2] row_mask:0xf bank_mask:0xf bound_ctrl:1
	v_cvt_f32_f16_e32 v92, v77
	v_cvt_f32_f16_sdwa v93, v77 dst_sel:DWORD dst_unused:UNUSED_PAD src0_sel:WORD_1
	v_add_f32_dpp v34, v34, v34 quad_perm:[2,3,0,1] row_mask:0xf bank_mask:0xf bound_ctrl:1
	v_cvt_f32_f16_e32 v96, v72
	v_cvt_f32_f16_sdwa v97, v72 dst_sel:DWORD dst_unused:UNUSED_PAD src0_sel:WORD_1
	v_add_f32_dpp v34, v34, v34 row_half_mirror row_mask:0xf bank_mask:0xf bound_ctrl:1
	v_mul_f32_e32 v34, 0x3c800000, v34
	v_cvt_f32_f16_e32 v72, v76
	v_cvt_f32_f16_sdwa v73, v76 dst_sel:DWORD dst_unused:UNUSED_PAD src0_sel:WORD_1
	v_pk_add_f32 v[76:77], v[94:95], v[34:35] op_sel_hi:[1,0] neg_lo:[0,1] neg_hi:[0,1]
	v_pk_add_f32 v[78:79], v[78:79], v[34:35] op_sel_hi:[1,0] neg_lo:[0,1] neg_hi:[0,1]
	v_pk_mul_f32 v[94:95], v[76:77], v[76:77]
	v_pk_mul_f32 v[98:99], v[78:79], v[78:79]
	v_pk_add_f32 v[86:87], v[86:87], v[34:35] op_sel_hi:[1,0] neg_lo:[0,1] neg_hi:[0,1]
	v_pk_add_f32 v[80:81], v[80:81], v[34:35] op_sel_hi:[1,0] neg_lo:[0,1] neg_hi:[0,1]
	v_add_f32_e32 v34, v94, v95
	v_add_f32_e32 v34, v98, v34
	v_pk_mul_f32 v[100:101], v[86:87], v[86:87]
	v_add_f32_e32 v34, v99, v34
	v_add_f32_e32 v34, v100, v34
	v_pk_mul_f32 v[102:103], v[80:81], v[80:81]
	v_add_f32_e32 v34, v101, v34
	v_add_f32_e32 v34, v102, v34
	v_add_f32_e32 v34, v103, v34
	v_and_b32_e32 v38, 0xffff0000, v37
	v_and_b32_e32 v42, 0xffff0000, v41
	v_add_f32_dpp v34, v34, v34 quad_perm:[1,0,3,2] row_mask:0xf bank_mask:0xf bound_ctrl:1
	s_waitcnt vmcnt(6)
	v_cvt_f32_f16_e32 v40, v57
	v_cvt_f32_f16_e32 v36, v56
	v_add_f32_dpp v34, v34, v34 quad_perm:[2,3,0,1] row_mask:0xf bank_mask:0xf bound_ctrl:1
	v_and_b32_e32 v46, 0xffff0000, v45
	v_and_b32_e32 v50, 0xffff0000, v49
	v_add_f32_dpp v34, v34, v34 row_half_mirror row_mask:0xf bank_mask:0xf bound_ctrl:1
	v_fmamk_f32 v34, v34, 0x3c800000, v216
	v_rsq_f32_e32 v34, v34
	v_cvt_f32_f16_e32 v48, v59
	v_cvt_f32_f16_e32 v44, v58
	v_pk_mul_f32 v[76:77], v[76:77], v[34:35] op_sel_hi:[1,0]
	s_nop 0
	v_pk_fma_f32 v[76:77], v[10:11], v[76:77], v[2:3]
	s_nop 0
	v_pk_fma_f32 v[76:77], v[52:53], v[96:97], v[76:77] op_sel:[1,0,0]
	s_nop 0
	v_pk_mul_f32 v[72:73], v[76:77], v[72:73]
	v_pk_mul_f32 v[76:77], v[78:79], v[34:35] op_sel_hi:[1,0]
	v_pk_mul_f32 v[78:79], v[86:87], v[34:35] op_sel_hi:[1,0]
	v_pk_fma_f32 v[76:77], v[12:13], v[76:77], v[4:5]
	v_pk_fma_f32 v[78:79], v[14:15], v[78:79], v[6:7]
	v_pk_fma_f32 v[76:77], v[52:53], v[90:91], v[76:77] op_sel:[1,0,0]
	v_pk_fma_f32 v[78:79], v[52:53], v[88:89], v[78:79] op_sel:[1,0,0]
	v_pk_mul_f32 v[76:77], v[76:77], v[92:93]
	v_pk_mul_f32 v[74:75], v[78:79], v[74:75]
	v_pk_mul_f32 v[78:79], v[80:81], v[34:35] op_sel_hi:[1,0]
	v_cvt_pk_bf16_f32 v72, v72, v73
	v_pk_fma_f32 v[78:79], v[16:17], v[78:79], v[8:9]
	v_cvt_pk_bf16_f32 v73, v76, v77
	v_pk_fma_f32 v[52:53], v[52:53], v[82:83], v[78:79] op_sel:[1,0,0]
	v_cvt_pk_bf16_f32 v74, v74, v75
	v_pk_mul_f32 v[52:53], v[52:53], v[84:85]
	v_lshlrev_b32_e32 v84, 16, v37
	v_cvt_pk_bf16_f32 v75, v52, v53
	v_lshl_add_u64 v[52:53], v[144:145], 0, s[26:27]
	v_lshlrev_b32_e32 v85, 16, v39
	v_add_f32_e32 v34, 0, v84
	global_store_dwordx4 v[52:53], v[72:75], off
	v_cvt_f32_f16_e32 v78, v66
	v_cvt_f32_f16_sdwa v79, v66 dst_sel:DWORD dst_unused:UNUSED_PAD src0_sel:WORD_1
	v_cvt_f32_f16_e32 v72, v67
	v_cvt_f32_f16_sdwa v73, v67 dst_sel:DWORD dst_unused:UNUSED_PAD src0_sel:WORD_1
	v_cvt_f32_f16_e32 v66, v70
	v_cvt_f32_f16_sdwa v67, v70 dst_sel:DWORD dst_unused:UNUSED_PAD src0_sel:WORD_1
	v_lshlrev_b32_e32 v70, 16, v41
	v_add_f32_e32 v34, v34, v85
	v_cvt_f32_f16_e32 v74, v71
	v_cvt_f32_f16_sdwa v75, v71 dst_sel:DWORD dst_unused:UNUSED_PAD src0_sel:WORD_1
	v_lshlrev_b32_e32 v71, 16, v43
	v_add_f32_e32 v34, v34, v70
	v_lshlrev_b32_e32 v76, 16, v45
	v_add_f32_e32 v34, v34, v71
	v_lshlrev_b32_e32 v77, 16, v47
	v_add_f32_e32 v34, v34, v76
	v_lshlrev_b32_e32 v52, 16, v49
	v_add_f32_e32 v34, v34, v77
	v_lshlrev_b32_e32 v53, 16, v51
	v_add_f32_e32 v34, v34, v52
	v_add_f32_e32 v34, v34, v53
	v_cvt_f32_f16_e32 v80, v65
	v_cvt_f32_f16_sdwa v81, v65 dst_sel:DWORD dst_unused:UNUSED_PAD src0_sel:WORD_1
	v_add_f32_dpp v34, v34, v34 quad_perm:[1,0,3,2] row_mask:0xf bank_mask:0xf bound_ctrl:1
	v_cvt_f32_f16_e32 v82, v69
	v_cvt_f32_f16_sdwa v83, v69 dst_sel:DWORD dst_unused:UNUSED_PAD src0_sel:WORD_1
	v_add_f32_dpp v34, v34, v34 quad_perm:[2,3,0,1] row_mask:0xf bank_mask:0xf bound_ctrl:1
	v_cvt_f32_f16_e32 v86, v64
	v_cvt_f32_f16_sdwa v87, v64 dst_sel:DWORD dst_unused:UNUSED_PAD src0_sel:WORD_1
	v_add_f32_dpp v34, v34, v34 row_half_mirror row_mask:0xf bank_mask:0xf bound_ctrl:1
	v_mul_f32_e32 v34, 0x3c800000, v34
	v_cvt_f32_f16_e32 v64, v68
	v_cvt_f32_f16_sdwa v65, v68 dst_sel:DWORD dst_unused:UNUSED_PAD src0_sel:WORD_1
	v_pk_add_f32 v[68:69], v[84:85], v[34:35] op_sel_hi:[1,0] neg_lo:[0,1] neg_hi:[0,1]
	v_pk_add_f32 v[70:71], v[70:71], v[34:35] op_sel_hi:[1,0] neg_lo:[0,1] neg_hi:[0,1]
	v_pk_mul_f32 v[84:85], v[68:69], v[68:69]
	v_pk_mul_f32 v[88:89], v[70:71], v[70:71]
	v_pk_add_f32 v[76:77], v[76:77], v[34:35] op_sel_hi:[1,0] neg_lo:[0,1] neg_hi:[0,1]
	v_pk_add_f32 v[52:53], v[52:53], v[34:35] op_sel_hi:[1,0] neg_lo:[0,1] neg_hi:[0,1]
	v_add_f32_e32 v34, v84, v85
	v_add_f32_e32 v34, v88, v34
	v_pk_mul_f32 v[90:91], v[76:77], v[76:77]
	v_add_f32_e32 v34, v89, v34
	v_add_f32_e32 v34, v90, v34
	v_pk_mul_f32 v[92:93], v[52:53], v[52:53]
	v_add_f32_e32 v34, v91, v34
	v_add_f32_e32 v34, v92, v34
	v_add_f32_e32 v34, v93, v34
	v_cvt_f32_f16_sdwa v41, v57 dst_sel:DWORD dst_unused:UNUSED_PAD src0_sel:WORD_1
	v_and_b32_e32 v39, 0xffff0000, v39
	v_add_f32_dpp v34, v34, v34 quad_perm:[1,0,3,2] row_mask:0xf bank_mask:0xf bound_ctrl:1
	v_cvt_f32_f16_sdwa v37, v56 dst_sel:DWORD dst_unused:UNUSED_PAD src0_sel:WORD_1
	s_waitcnt vmcnt(6)
	v_cvt_f32_f16_e32 v56, v60
	v_add_f32_dpp v34, v34, v34 quad_perm:[2,3,0,1] row_mask:0xf bank_mask:0xf bound_ctrl:1
	v_cvt_f32_f16_sdwa v57, v60 dst_sel:DWORD dst_unused:UNUSED_PAD src0_sel:WORD_1
	v_add_f32_e32 v60, 0, v38
	v_add_f32_dpp v34, v34, v34 row_half_mirror row_mask:0xf bank_mask:0xf bound_ctrl:1
	v_fmamk_f32 v34, v34, 0x3c800000, v216
	v_rsq_f32_e32 v34, v34
	v_add_f32_e32 v60, v60, v39
	v_and_b32_e32 v43, 0xffff0000, v43
	v_add_f32_e32 v60, v60, v42
	v_add_f32_e32 v60, v60, v43
	v_and_b32_e32 v47, 0xffff0000, v47
	v_add_f32_e32 v60, v60, v46
	v_pk_mul_f32 v[68:69], v[68:69], v[34:35] op_sel_hi:[1,0]
	v_add_f32_e32 v60, v60, v47
	v_pk_fma_f32 v[68:69], v[10:11], v[68:69], v[2:3]
	v_and_b32_e32 v51, 0xffff0000, v51
	v_add_f32_e32 v60, v60, v50
	v_pk_fma_f32 v[68:69], v[54:55], v[86:87], v[68:69] op_sel_hi:[0,1,1]
	v_add_f32_e32 v60, v60, v51
	v_pk_mul_f32 v[64:65], v[68:69], v[64:65]
	v_pk_mul_f32 v[68:69], v[70:71], v[34:35] op_sel_hi:[1,0]
	v_pk_mul_f32 v[70:71], v[76:77], v[34:35] op_sel_hi:[1,0]
	v_pk_mul_f32 v[52:53], v[52:53], v[34:35] op_sel_hi:[1,0]
	v_add_f32_dpp v60, v60, v60 quad_perm:[1,0,3,2] row_mask:0xf bank_mask:0xf bound_ctrl:1
	v_pk_fma_f32 v[68:69], v[12:13], v[68:69], v[4:5]
	v_pk_fma_f32 v[70:71], v[14:15], v[70:71], v[6:7]
	v_pk_fma_f32 v[52:53], v[16:17], v[52:53], v[8:9]
	v_add_f32_dpp v60, v60, v60 quad_perm:[2,3,0,1] row_mask:0xf bank_mask:0xf bound_ctrl:1
	v_pk_fma_f32 v[68:69], v[54:55], v[80:81], v[68:69] op_sel_hi:[0,1,1]
	v_pk_fma_f32 v[70:71], v[54:55], v[78:79], v[70:71] op_sel_hi:[0,1,1]
	v_pk_fma_f32 v[52:53], v[54:55], v[72:73], v[52:53] op_sel_hi:[0,1,1]
	v_add_f32_dpp v60, v60, v60 row_half_mirror row_mask:0xf bank_mask:0xf bound_ctrl:1
	v_pk_mul_f32 v[68:69], v[68:69], v[82:83]
	v_pk_mul_f32 v[66:67], v[70:71], v[66:67]
	v_pk_mul_f32 v[52:53], v[52:53], v[74:75]
	v_mul_f32_e32 v60, 0x3c800000, v60
	v_cvt_pk_bf16_f32 v64, v64, v65
	v_cvt_pk_bf16_f32 v65, v68, v69
	v_cvt_pk_bf16_f32 v66, v66, v67
	v_cvt_pk_bf16_f32 v67, v52, v53
	v_lshl_add_u64 v[52:53], v[144:145], 0, s[28:29]
	v_pk_add_f32 v[38:39], v[38:39], v[60:61] op_sel_hi:[1,0] neg_lo:[0,1] neg_hi:[0,1]
	global_store_dwordx4 v[52:53], v[64:67], off
	v_cvt_f32_f16_sdwa v49, v59 dst_sel:DWORD dst_unused:UNUSED_PAD src0_sel:WORD_1
	v_cvt_f32_f16_e32 v52, v63
	v_cvt_f32_f16_sdwa v53, v63 dst_sel:DWORD dst_unused:UNUSED_PAD src0_sel:WORD_1
	v_cvt_f32_f16_sdwa v45, v58 dst_sel:DWORD dst_unused:UNUSED_PAD src0_sel:WORD_1
	v_cvt_f32_f16_e32 v58, v62
	v_cvt_f32_f16_sdwa v59, v62 dst_sel:DWORD dst_unused:UNUSED_PAD src0_sel:WORD_1
	v_pk_mul_f32 v[62:63], v[38:39], v[38:39]
	v_pk_add_f32 v[42:43], v[42:43], v[60:61] op_sel_hi:[1,0] neg_lo:[0,1] neg_hi:[0,1]
	v_add_f32_e32 v62, v62, v63
	v_pk_mul_f32 v[64:65], v[42:43], v[42:43]
	v_pk_add_f32 v[46:47], v[46:47], v[60:61] op_sel_hi:[1,0] neg_lo:[0,1] neg_hi:[0,1]
	v_add_f32_e32 v62, v64, v62
	v_pk_mul_f32 v[66:67], v[46:47], v[46:47]
	v_add_f32_e32 v62, v65, v62
	v_pk_add_f32 v[50:51], v[50:51], v[60:61] op_sel_hi:[1,0] neg_lo:[0,1] neg_hi:[0,1]
	v_add_f32_e32 v62, v66, v62
	v_mov_b32_e32 v34, v55
	v_cvt_f32_f16_e32 v54, v61
	v_cvt_f32_f16_sdwa v55, v61 dst_sel:DWORD dst_unused:UNUSED_PAD src0_sel:WORD_1
	v_pk_mul_f32 v[60:61], v[50:51], v[50:51]
	v_add_f32_e32 v62, v67, v62
	v_add_f32_e32 v60, v60, v62
	v_add_f32_e32 v60, v61, v60
	s_nop 1
	v_add_f32_dpp v60, v60, v60 quad_perm:[1,0,3,2] row_mask:0xf bank_mask:0xf bound_ctrl:1
	s_nop 1
	v_add_f32_dpp v60, v60, v60 quad_perm:[2,3,0,1] row_mask:0xf bank_mask:0xf bound_ctrl:1
	s_nop 1
	v_add_f32_dpp v60, v60, v60 row_half_mirror row_mask:0xf bank_mask:0xf bound_ctrl:1
	v_fmamk_f32 v60, v60, 0x3c800000, v216
	v_rsq_f32_e32 v60, v60
	s_nop 0
	v_pk_mul_f32 v[38:39], v[38:39], v[60:61] op_sel_hi:[1,0]
	s_nop 0
	v_pk_fma_f32 v[38:39], v[10:11], v[38:39], v[2:3]
	s_nop 0
	v_pk_fma_f32 v[36:37], v[34:35], v[36:37], v[38:39] op_sel_hi:[0,1,1]
	v_pk_mul_f32 v[38:39], v[42:43], v[60:61] op_sel_hi:[1,0]
	v_pk_mul_f32 v[42:43], v[50:51], v[60:61] op_sel_hi:[1,0]
	v_pk_fma_f32 v[38:39], v[12:13], v[38:39], v[4:5]
	v_pk_fma_f32 v[42:43], v[16:17], v[42:43], v[8:9]
	v_pk_fma_f32 v[38:39], v[34:35], v[40:41], v[38:39] op_sel_hi:[0,1,1]
	v_pk_mul_f32 v[40:41], v[46:47], v[60:61] op_sel_hi:[1,0]
	v_pk_fma_f32 v[42:43], v[34:35], v[48:49], v[42:43] op_sel_hi:[0,1,1]
	v_pk_fma_f32 v[40:41], v[14:15], v[40:41], v[6:7]
	v_pk_mul_f32 v[36:37], v[36:37], v[56:57]
	v_pk_fma_f32 v[40:41], v[34:35], v[44:45], v[40:41] op_sel_hi:[0,1,1]
	v_pk_mul_f32 v[38:39], v[38:39], v[54:55]
	v_pk_mul_f32 v[40:41], v[40:41], v[58:59]
	v_pk_mul_f32 v[42:43], v[42:43], v[52:53]
	v_cvt_pk_bf16_f32 v36, v36, v37
	v_cvt_pk_bf16_f32 v37, v38, v39
	v_cvt_pk_bf16_f32 v38, v40, v41
	v_cvt_pk_bf16_f32 v39, v42, v43
	v_lshl_add_u64 v[40:41], v[144:145], 0, s[30:31]
	global_store_dwordx4 v[40:41], v[36:39], off
	s_cbranch_scc1 .LBB0_553

.LBB0_840:
	s_ashr_i32 s5, s4, 31
	s_lshl_b64 s[14:15], s[4:5], 13
	v_lshl_add_u64 v[2:3], v[72:73], 0, s[14:15]
	global_load_dwordx4 v[74:77], v[2:3], off nt
	global_load_dwordx4 v[78:81], v[2:3], off offset:1024 nt
	global_load_dwordx4 v[56:59], v[2:3], off offset:2048 nt
	global_load_dwordx4 v[52:55], v[2:3], off offset:3072 nt
	v_add_co_u32_e32 v2, vcc, s73, v2
	s_add_i32 s18, s4, s22
	s_nop 0
	v_addc_co_u32_e32 v3, vcc, 0, v3, vcc
	global_load_dwordx4 v[48:51], v[2:3], off nt
	global_load_dwordx4 v[44:47], v[2:3], off offset:1024 nt
	global_load_dwordx4 v[36:39], v[2:3], off offset:3072 nt
	global_load_dwordx4 v[40:43], v[2:3], off offset:2048 nt
	global_load_dwordx4 v[82:85], v[62:63], off nt
	s_cmp_lt_i32 s18, 0x8000
	s_cselect_b32 s14, s18, s4
	s_ashr_i32 s15, s14, 31
	s_lshl_b64 s[14:15], s[14:15], 13
	s_lshl_b64 s[4:5], s[4:5], 12
	v_lshl_add_u64 v[2:3], v[72:73], 0, s[14:15]
	s_add_u32 s4, s23, s4
	v_lshlrev_b32_e32 v61, 3, v60
	s_addc_u32 s5, s24, s5
	s_cmpk_gt_i32 s18, 0x7fff
	s_waitcnt vmcnt(0)
	v_mov_b32_e32 v6, v75
	v_mov_b32_e32 v7, v79
	v_mov_b32_e32 v10, v77
	v_mov_b32_e32 v11, v81
	v_mov_b32_e32 v4, v74
	v_mov_b32_e32 v5, v78
	v_mov_b32_e32 v8, v76
	v_mov_b32_e32 v9, v80
	v_pk_mul_f32 v[12:13], v[58:59], v[58:59]
	v_pk_mul_f32 v[14:15], v[56:57], v[56:57]
	v_pk_mul_f32 v[6:7], v[6:7], v[6:7]
	v_pk_mul_f32 v[10:11], v[10:11], v[10:11]
	v_pk_mov_b32 v[20:21], v[14:15], v[12:13] op_sel:[1,0]
	v_mov_b32_e32 v15, v13
	v_pk_fma_f32 v[4:5], v[4:5], v[4:5], v[6:7]
	v_pk_fma_f32 v[6:7], v[8:9], v[8:9], v[10:11]
	v_mul_f32_e32 v16, v53, v53
	v_mul_f32_e32 v18, v55, v55
	v_pk_add_f32 v[8:9], v[20:21], v[14:15]
	v_pk_add_f32 v[4:5], v[4:5], v[6:7]
	v_mul_f32_e32 v25, v48, v48
	v_mul_f32_e32 v27, v49, v49
	v_mul_f32_e32 v28, v50, v50
	v_mul_f32_e32 v29, v51, v51
	v_pk_fma_f32 v[12:13], v[52:53], v[52:53], v[16:17] op_sel_hi:[1,1,0]
	v_pk_fma_f32 v[16:17], v[54:55], v[54:55], v[18:19] op_sel_hi:[1,1,0]
	v_pk_add_f32 v[6:7], v[8:9], v[8:9] op_sel:[0,1] op_sel_hi:[1,0]
	v_pk_add_f32 v[4:5], v[4:5], v[4:5] op_sel:[0,1] op_sel_hi:[1,0]
	v_pk_mul_f32 v[18:19], v[46:47], v[46:47]
	v_pk_mul_f32 v[22:23], v[44:45], v[44:45]
	v_mov_b32_e32 v13, v28
	v_mov_b32_e32 v17, v29
	v_mov_b32_e32 v7, v27
	v_mov_b32_e32 v5, v25
	v_pk_mov_b32 v[10:11], v[22:23], v[18:19] op_sel:[1,0]
	v_mov_b32_e32 v23, v19
	v_pk_add_f32 v[8:9], v[12:13], v[16:17]
	v_pk_add_f32 v[4:5], v[4:5], v[6:7]
	v_mul_f32_e32 v24, v41, v41
	v_mul_f32_e32 v26, v43, v43
	v_pk_add_f32 v[10:11], v[10:11], v[22:23]
	v_pk_add_f32 v[4:5], v[4:5], v[8:9]
	v_mul_f32_e32 v30, v36, v36
	v_mul_f32_e32 v31, v37, v37
	v_mul_f32_e32 v32, v38, v38
	v_mul_f32_e32 v33, v39, v39
	v_pk_fma_f32 v[14:15], v[40:41], v[40:41], v[24:25] op_sel_hi:[1,1,0]
	v_pk_fma_f32 v[18:19], v[42:43], v[42:43], v[26:27] op_sel_hi:[1,1,0]
	v_pk_add_f32 v[10:11], v[10:11], v[10:11] op_sel:[0,1] op_sel_hi:[1,0]
	v_pk_add_f32 v[4:5], v[4:5], v[4:5] op_sel:[0,1] op_sel_hi:[1,0]
	v_mov_b32_e32 v15, v32
	v_mov_b32_e32 v19, v33
	v_mov_b32_e32 v11, v31
	v_mov_b32_e32 v5, v30
	v_pk_add_f32 v[12:13], v[14:15], v[18:19]
	v_pk_add_f32 v[4:5], v[4:5], v[10:11]
	global_load_dwordx4 v[30:33], v[2:3], off nt
	global_load_dwordx4 v[26:29], v[2:3], off offset:1024 nt
	global_load_dwordx4 v[22:25], v[2:3], off offset:2048 nt
	global_load_dwordx4 v[18:21], v[2:3], off offset:3072 nt
	v_pk_add_f32 v[4:5], v[4:5], v[12:13]
	v_add_co_u32_e32 v2, vcc, s73, v2
	v_add_f32_e32 v4, v4, v5
	s_nop 0
	v_addc_co_u32_e32 v3, vcc, 0, v3, vcc
	v_add_f32_dpp v4, v4, v4 quad_perm:[1,0,3,2] row_mask:0xf bank_mask:0xf bound_ctrl:1
	s_nop 1
	v_add_f32_dpp v4, v4, v4 quad_perm:[2,3,0,1] row_mask:0xf bank_mask:0xf bound_ctrl:1
	s_nop 1
	v_add_f32_dpp v4, v4, v4 row_half_mirror row_mask:0xf bank_mask:0xf bound_ctrl:1
	s_nop 1
	v_add_f32_dpp v4, v4, v4 row_mirror row_mask:0xf bank_mask:0xf bound_ctrl:1
	ds_swizzle_b32 v5, v4 offset:swizzle(SWAP,16)
	s_waitcnt lgkmcnt(0)
	v_add_f32_e32 v4, v4, v5
	ds_bpermute_b32 v5, v1, v4
	s_waitcnt lgkmcnt(0)
	v_add_f32_e32 v4, v4, v5
	v_fmamk_f32 v4, v4, 0x3a000000, v214
	v_rsq_f32_e32 v34, v4
	global_load_dwordx4 v[14:17], v[2:3], off nt
	global_load_dwordx4 v[10:13], v[2:3], off offset:1024 nt
	global_load_dwordx4 v[6:9], v[2:3], off offset:2048 nt
	s_nop 0
	global_load_dwordx4 v[2:5], v[2:3], off offset:3072 nt
	v_pk_mul_f32 v[74:75], v[74:75], v[34:35] op_sel_hi:[1,0]
	v_pk_mul_f32 v[76:77], v[76:77], v[34:35] op_sel_hi:[1,0]
	v_pk_mul_f32 v[74:75], v[82:83], v[74:75]
	v_pk_mul_f32 v[76:77], v[84:85], v[76:77]
	v_cvt_pk_bf16_f32 v74, v74, v75
	v_cvt_pk_bf16_f32 v75, v76, v77
	global_store_dwordx2 v61, v[74:75], s[4:5]
	global_load_dwordx4 v[74:77], v[62:63], off offset:1024 nt
	v_pk_mul_f32 v[78:79], v[78:79], v[34:35] op_sel_hi:[1,0]
	v_pk_mul_f32 v[80:81], v[80:81], v[34:35] op_sel_hi:[1,0]
	v_pk_mul_f32 v[56:57], v[56:57], v[34:35] op_sel_hi:[1,0]
	v_pk_mul_f32 v[58:59], v[58:59], v[34:35] op_sel_hi:[1,0]
	v_pk_mul_f32 v[52:53], v[52:53], v[34:35] op_sel_hi:[1,0]
	v_pk_mul_f32 v[54:55], v[54:55], v[34:35] op_sel_hi:[1,0]
	v_pk_mul_f32 v[48:49], v[48:49], v[34:35] op_sel_hi:[1,0]
	v_pk_mul_f32 v[50:51], v[50:51], v[34:35] op_sel_hi:[1,0]
	v_pk_mul_f32 v[44:45], v[44:45], v[34:35] op_sel_hi:[1,0]
	v_pk_mul_f32 v[46:47], v[46:47], v[34:35] op_sel_hi:[1,0]
	v_pk_mul_f32 v[40:41], v[40:41], v[34:35] op_sel_hi:[1,0]
	v_pk_mul_f32 v[42:43], v[42:43], v[34:35] op_sel_hi:[1,0]
	v_pk_mul_f32 v[36:37], v[36:37], v[34:35] op_sel_hi:[1,0]
	v_pk_mul_f32 v[38:39], v[38:39], v[34:35] op_sel_hi:[1,0]
	s_waitcnt vmcnt(0)
	v_pk_mul_f32 v[74:75], v[74:75], v[78:79]
	v_pk_mul_f32 v[76:77], v[76:77], v[80:81]
	v_cvt_pk_bf16_f32 v74, v74, v75
	v_cvt_pk_bf16_f32 v75, v76, v77
	global_store_dwordx2 v61, v[74:75], s[4:5] offset:512
	global_load_dwordx4 v[74:77], v[62:63], off offset:2048 nt
	s_waitcnt vmcnt(0)
	v_pk_mul_f32 v[56:57], v[74:75], v[56:57]
	v_pk_mul_f32 v[58:59], v[76:77], v[58:59]
	v_cvt_pk_bf16_f32 v56, v56, v57
	v_cvt_pk_bf16_f32 v57, v58, v59
	global_store_dwordx2 v61, v[56:57], s[4:5] offset:1024
	global_load_dwordx4 v[56:59], v[62:63], off offset:3072 nt
	s_waitcnt vmcnt(0)
	v_pk_mul_f32 v[52:53], v[52:53], v[56:57]
	v_pk_mul_f32 v[54:55], v[54:55], v[58:59]
	v_cvt_pk_bf16_f32 v52, v52, v53
	v_cvt_pk_bf16_f32 v53, v54, v55
	global_store_dwordx2 v61, v[52:53], s[4:5] offset:1536
	global_load_dwordx4 v[52:55], v[64:65], off nt
	s_waitcnt vmcnt(0)
	v_pk_mul_f32 v[48:49], v[48:49], v[52:53]
	v_pk_mul_f32 v[50:51], v[50:51], v[54:55]
	v_cvt_pk_bf16_f32 v48, v48, v49
	v_cvt_pk_bf16_f32 v49, v50, v51
	global_store_dwordx2 v61, v[48:49], s[4:5] offset:2048
	global_load_dwordx4 v[48:51], v[66:67], off nt
	s_waitcnt vmcnt(0)
	v_pk_mul_f32 v[44:45], v[44:45], v[48:49]
	v_pk_mul_f32 v[46:47], v[46:47], v[50:51]
	v_cvt_pk_bf16_f32 v44, v44, v45
	v_cvt_pk_bf16_f32 v45, v46, v47
	global_store_dwordx2 v61, v[44:45], s[4:5] offset:2560
	global_load_dwordx4 v[44:47], v[68:69], off nt
	s_waitcnt vmcnt(0)
	v_pk_mul_f32 v[40:41], v[40:41], v[44:45]
	v_pk_mul_f32 v[42:43], v[42:43], v[46:47]
	v_cvt_pk_bf16_f32 v40, v40, v41
	v_cvt_pk_bf16_f32 v41, v42, v43
	global_store_dwordx2 v61, v[40:41], s[4:5] offset:3072
	global_load_dwordx4 v[40:43], v[70:71], off nt
	s_waitcnt vmcnt(0)
	v_pk_mul_f32 v[36:37], v[36:37], v[40:41]
	v_pk_mul_f32 v[38:39], v[38:39], v[42:43]
	v_cvt_pk_bf16_f32 v36, v36, v37
	v_cvt_pk_bf16_f32 v37, v38, v39
	global_store_dwordx2 v61, v[36:37], s[4:5] offset:3584
	s_cbranch_scc1 .LBB0_839
	v_mov_b32_e32 v38, v31
	v_mov_b32_e32 v39, v27
	v_mov_b32_e32 v36, v30
	v_mov_b32_e32 v37, v26
	v_pk_mul_f32 v[38:39], v[38:39], v[38:39]
	v_mov_b32_e32 v40, v33
	v_mov_b32_e32 v41, v29
	v_pk_fma_f32 v[36:37], v[36:37], v[36:37], v[38:39]
	v_mov_b32_e32 v38, v32
	v_mov_b32_e32 v39, v28
	v_pk_mul_f32 v[40:41], v[40:41], v[40:41]
	v_mul_f32_e32 v34, v14, v14
	v_pk_fma_f32 v[38:39], v[38:39], v[38:39], v[40:41]
	v_pk_mul_f32 v[40:41], v[22:23], v[22:23]
	v_pk_add_f32 v[36:37], v[36:37], v[38:39]
	v_pk_mul_f32 v[38:39], v[24:25], v[24:25]
	v_pk_add_f32 v[36:37], v[36:37], v[36:37] op_sel:[0,1] op_sel_hi:[1,0]
	v_pk_mov_b32 v[42:43], v[40:41], v[38:39] op_sel:[1,0]
	v_mov_b32_e32 v41, v39
	v_pk_add_f32 v[38:39], v[42:43], v[40:41]
	v_mul_f32_e32 v40, v15, v15
	v_pk_add_f32 v[38:39], v[38:39], v[38:39] op_sel:[0,1] op_sel_hi:[1,0]
	v_mov_b32_e32 v37, v34
	v_mov_b32_e32 v39, v40
	v_mul_f32_e32 v34, v19, v19
	v_mul_f32_e32 v41, v16, v16
	v_pk_add_f32 v[36:37], v[36:37], v[38:39]
	v_pk_fma_f32 v[38:39], v[18:19], v[18:19], v[34:35] op_sel_hi:[1,1,0]
	v_mul_f32_e32 v34, v21, v21
	v_mul_f32_e32 v42, v17, v17
	v_mov_b32_e32 v39, v41
	v_pk_fma_f32 v[40:41], v[20:21], v[20:21], v[34:35] op_sel_hi:[1,1,0]
	v_mul_f32_e32 v34, v2, v2
	v_mov_b32_e32 v41, v42
	v_pk_add_f32 v[38:39], v[38:39], v[40:41]
	v_pk_mul_f32 v[40:41], v[10:11], v[10:11]
	v_pk_add_f32 v[36:37], v[36:37], v[38:39]
	v_pk_mul_f32 v[38:39], v[12:13], v[12:13]
	v_pk_add_f32 v[36:37], v[36:37], v[36:37] op_sel:[0,1] op_sel_hi:[1,0]
	v_pk_mov_b32 v[42:43], v[40:41], v[38:39] op_sel:[1,0]
	v_mov_b32_e32 v41, v39
	v_pk_add_f32 v[38:39], v[42:43], v[40:41]
	v_mul_f32_e32 v40, v3, v3
	v_pk_add_f32 v[38:39], v[38:39], v[38:39] op_sel:[0,1] op_sel_hi:[1,0]
	v_mov_b32_e32 v37, v34
	v_mov_b32_e32 v39, v40
	v_mul_f32_e32 v34, v7, v7
	v_mul_f32_e32 v41, v4, v4
	v_pk_add_f32 v[36:37], v[36:37], v[38:39]
	v_pk_fma_f32 v[38:39], v[6:7], v[6:7], v[34:35] op_sel_hi:[1,1,0]
	v_mul_f32_e32 v34, v9, v9
	v_mul_f32_e32 v42, v5, v5
	v_mov_b32_e32 v39, v41
	v_pk_fma_f32 v[40:41], v[8:9], v[8:9], v[34:35] op_sel_hi:[1,1,0]
	s_ashr_i32 s19, s18, 31
	v_mov_b32_e32 v41, v42
	v_pk_add_f32 v[38:39], v[38:39], v[40:41]
	s_lshl_b64 s[4:5], s[18:19], 12
	v_pk_add_f32 v[36:37], v[36:37], v[38:39]
	s_add_u32 s20, s23, s4
	v_add_f32_e32 v34, v36, v37
	s_addc_u32 s21, s24, s5
	s_nop 0
	v_add_f32_dpp v34, v34, v34 quad_perm:[1,0,3,2] row_mask:0xf bank_mask:0xf bound_ctrl:1
	s_nop 1
	v_add_f32_dpp v34, v34, v34 quad_perm:[2,3,0,1] row_mask:0xf bank_mask:0xf bound_ctrl:1
	s_nop 1
	v_add_f32_dpp v34, v34, v34 row_half_mirror row_mask:0xf bank_mask:0xf bound_ctrl:1
	s_nop 1
	v_add_f32_dpp v34, v34, v34 row_mirror row_mask:0xf bank_mask:0xf bound_ctrl:1
	ds_swizzle_b32 v36, v34 offset:swizzle(SWAP,16)
	s_waitcnt lgkmcnt(0)
	v_add_f32_e32 v34, v34, v36
	ds_bpermute_b32 v36, v1, v34
	s_waitcnt lgkmcnt(0)
	v_add_f32_e32 v34, v34, v36
	global_load_dwordx4 v[36:39], v[62:63], off nt
	v_fmamk_f32 v34, v34, 0x3a000000, v214
	v_rsq_f32_e32 v34, v34
	s_nop 0
	v_pk_mul_f32 v[30:31], v[30:31], v[34:35] op_sel_hi:[1,0]
	v_pk_mul_f32 v[32:33], v[32:33], v[34:35] op_sel_hi:[1,0]
	v_pk_mul_f32 v[26:27], v[26:27], v[34:35] op_sel_hi:[1,0]
	v_pk_mul_f32 v[28:29], v[28:29], v[34:35] op_sel_hi:[1,0]
	v_pk_mul_f32 v[22:23], v[22:23], v[34:35] op_sel_hi:[1,0]
	v_pk_mul_f32 v[24:25], v[24:25], v[34:35] op_sel_hi:[1,0]
	v_pk_mul_f32 v[18:19], v[18:19], v[34:35] op_sel_hi:[1,0]
	v_pk_mul_f32 v[20:21], v[20:21], v[34:35] op_sel_hi:[1,0]
	v_pk_mul_f32 v[14:15], v[14:15], v[34:35] op_sel_hi:[1,0]
	v_pk_mul_f32 v[16:17], v[16:17], v[34:35] op_sel_hi:[1,0]
	v_pk_mul_f32 v[10:11], v[10:11], v[34:35] op_sel_hi:[1,0]
	v_pk_mul_f32 v[12:13], v[12:13], v[34:35] op_sel_hi:[1,0]
	v_pk_mul_f32 v[6:7], v[6:7], v[34:35] op_sel_hi:[1,0]
	v_pk_mul_f32 v[8:9], v[8:9], v[34:35] op_sel_hi:[1,0]
	v_pk_mul_f32 v[2:3], v[2:3], v[34:35] op_sel_hi:[1,0]
	v_pk_mul_f32 v[4:5], v[4:5], v[34:35] op_sel_hi:[1,0]
	s_waitcnt vmcnt(0)
	v_pk_mul_f32 v[30:31], v[36:37], v[30:31]
	v_pk_mul_f32 v[32:33], v[38:39], v[32:33]
	v_cvt_pk_bf16_f32 v30, v30, v31
	v_cvt_pk_bf16_f32 v31, v32, v33
	global_store_dwordx2 v61, v[30:31], s[20:21]
	global_load_dwordx4 v[30:33], v[62:63], off offset:1024 nt
	s_waitcnt vmcnt(0)
	v_pk_mul_f32 v[26:27], v[30:31], v[26:27]
	v_pk_mul_f32 v[28:29], v[32:33], v[28:29]
	v_cvt_pk_bf16_f32 v26, v26, v27
	v_cvt_pk_bf16_f32 v27, v28, v29
	global_store_dwordx2 v61, v[26:27], s[20:21] offset:512
	global_load_dwordx4 v[26:29], v[62:63], off offset:2048 nt
	s_waitcnt vmcnt(0)
	v_pk_mul_f32 v[22:23], v[26:27], v[22:23]
	v_pk_mul_f32 v[24:25], v[28:29], v[24:25]
	v_cvt_pk_bf16_f32 v22, v22, v23
	v_cvt_pk_bf16_f32 v23, v24, v25
	global_store_dwordx2 v61, v[22:23], s[20:21] offset:1024
	global_load_dwordx4 v[22:25], v[62:63], off offset:3072 nt
	s_waitcnt vmcnt(0)
	v_pk_mul_f32 v[18:19], v[22:23], v[18:19]
	v_pk_mul_f32 v[20:21], v[24:25], v[20:21]
	v_cvt_pk_bf16_f32 v18, v18, v19
	v_cvt_pk_bf16_f32 v19, v20, v21
	global_store_dwordx2 v61, v[18:19], s[20:21] offset:1536
	global_load_dwordx4 v[18:21], v[64:65], off nt
	s_waitcnt vmcnt(0)
	v_pk_mul_f32 v[14:15], v[14:15], v[18:19]
	v_pk_mul_f32 v[16:17], v[16:17], v[20:21]
	v_cvt_pk_bf16_f32 v14, v14, v15
	v_cvt_pk_bf16_f32 v15, v16, v17
	global_store_dwordx2 v61, v[14:15], s[20:21] offset:2048
	global_load_dwordx4 v[14:17], v[66:67], off nt
	s_waitcnt vmcnt(0)
	v_pk_mul_f32 v[10:11], v[10:11], v[14:15]
	v_pk_mul_f32 v[12:13], v[12:13], v[16:17]
	v_cvt_pk_bf16_f32 v10, v10, v11
	v_cvt_pk_bf16_f32 v11, v12, v13
	global_store_dwordx2 v61, v[10:11], s[20:21] offset:2560
	global_load_dwordx4 v[10:13], v[68:69], off nt
	s_waitcnt vmcnt(0)
	v_pk_mul_f32 v[6:7], v[6:7], v[10:11]
	v_pk_mul_f32 v[8:9], v[8:9], v[12:13]
	v_cvt_pk_bf16_f32 v6, v6, v7
	v_cvt_pk_bf16_f32 v7, v8, v9
	global_store_dwordx2 v61, v[6:7], s[20:21] offset:3072
	global_load_dwordx4 v[6:9], v[70:71], off nt
	s_waitcnt vmcnt(0)
	v_pk_mul_f32 v[2:3], v[2:3], v[6:7]
	v_pk_mul_f32 v[4:5], v[4:5], v[8:9]
	v_cvt_pk_bf16_f32 v2, v2, v3
	v_cvt_pk_bf16_f32 v3, v4, v5
	global_store_dwordx2 v61, v[2:3], s[20:21] offset:3584
	s_branch .LBB0_839

	.amdhsa_kernel _Z8mega_fwdILi0ELi16EEv4Args
		.amdhsa_group_segment_fixed_size 0
		.amdhsa_private_segment_fixed_size 0
		.amdhsa_kernarg_size 528
		.amdhsa_user_sgpr_count 2
		.amdhsa_user_sgpr_dispatch_ptr 0
		.amdhsa_user_sgpr_queue_ptr 0
		.amdhsa_user_sgpr_kernarg_segment_ptr 1
		.amdhsa_user_sgpr_dispatch_id 0
		.amdhsa_user_sgpr_kernarg_preload_length 0
		.amdhsa_user_sgpr_kernarg_preload_offset 0
		.amdhsa_user_sgpr_private_segment_size 0
		.amdhsa_uses_dynamic_stack 0
		.amdhsa_enable_private_segment 0
		.amdhsa_system_sgpr_workgroup_id_x 1
		.amdhsa_system_sgpr_workgroup_id_y 0
		.amdhsa_system_sgpr_workgroup_id_z 0
		.amdhsa_system_sgpr_workgroup_info 0
		.amdhsa_system_vgpr_workitem_id 0
		.amdhsa_next_free_vgpr 255
		.amdhsa_next_free_sgpr 100
		.amdhsa_accum_offset 256
		.amdhsa_reserve_vcc 1
		.amdhsa_float_round_mode_32 0
		.amdhsa_float_round_mode_16_64 0
		.amdhsa_float_denorm_mode_32 3
		.amdhsa_float_denorm_mode_16_64 3
		.amdhsa_dx10_clamp 1
		.amdhsa_ieee_mode 1
		.amdhsa_fp16_overflow 0
		.amdhsa_tg_split 0
		.amdhsa_exception_fp_ieee_invalid_op 0
		.amdhsa_exception_fp_denorm_src 0
		.amdhsa_exception_fp_ieee_div_zero 0
		.amdhsa_exception_fp_ieee_overflow 0
		.amdhsa_exception_fp_ieee_underflow 0
		.amdhsa_exception_fp_ieee_inexact 0
		.amdhsa_exception_int_div_zero 0
	.end_amdhsa_kernel

amdhsa.kernels:
  - .agpr_count:     0
    .args:
      - .offset:         0
        .size:           272
        .value_kind:     by_value
      - .offset:         272
        .size:           4
        .value_kind:     hidden_block_count_x
      - .offset:         276
        .size:           4
        .value_kind:     hidden_block_count_y
      - .offset:         280
        .size:           4
        .value_kind:     hidden_block_count_z
      - .offset:         284
        .size:           2
        .value_kind:     hidden_group_size_x
      - .offset:         286
        .size:           2
        .value_kind:     hidden_group_size_y
      - .offset:         288
        .size:           2
        .value_kind:     hidden_group_size_z
      - .offset:         290
        .size:           2
        .value_kind:     hidden_remainder_x
      - .offset:         292
        .size:           2
        .value_kind:     hidden_remainder_y
      - .offset:         294
        .size:           2
        .value_kind:     hidden_remainder_z
      - .offset:         312
        .size:           8
        .value_kind:     hidden_global_offset_x
      - .offset:         320
        .size:           8
        .value_kind:     hidden_global_offset_y
      - .offset:         328
        .size:           8
        .value_kind:     hidden_global_offset_z
      - .offset:         336
        .size:           2
        .value_kind:     hidden_grid_dims
      - .offset:         392
        .size:           4
        .value_kind:     hidden_dynamic_lds_size
    .group_segment_fixed_size: 0
    .kernarg_segment_align: 8
    .kernarg_segment_size: 528
    .language:       OpenCL C
    .language_version:
      - 2
      - 0
    .max_flat_workgroup_size: 512
    .name:           _Z8mega_fwdILi0ELi16EEv4Args
    .private_segment_fixed_size: 0
    .sgpr_count:     106
    .sgpr_spill_count: 178
    .symbol:         _Z8mega_fwdILi0ELi16EEv4Args.kd
    .uniform_work_group_size: 1
    .uses_dynamic_stack: false
    .vgpr_count:     255
    .vgpr_spill_count: 0
    .wavefront_size: 64
